# baseline (speedup 1.0000x reference)
.LBB1_30:
	s_setprio 0
	s_load_dwordx8 s[8:15], s[0:1], 0x10
	s_load_dwordx2 s[16:17], s[0:1], 0x30
	s_bitcmp1_b32 s18, 6
	s_cselect_b32 s24, 0x60, 0
	s_lshr_b32 s4, s18, 1
	s_and_b32 s23, s4, 0x7fffffc0
	v_lshrrev_b32_e32 v98, 5, v1
	s_cmpk_lt_u32 s18, 0x200
	v_and_b32_e32 v1, 31, v0
	v_mov_b32_e32 v2, 0
	s_cselect_b64 s[4:5], -1, 0
	s_cmpk_gt_u32 s18, 0x1ff
	v_mov_b32_e32 v3, 0
	v_mov_b32_e32 v4, 0
	v_mov_b32_e32 v5, 0
	v_mov_b32_e32 v6, 0
	v_mov_b32_e32 v7, 0
	v_mov_b32_e32 v8, 0
	v_mov_b32_e32 v9, 0
	v_mov_b32_e32 v10, 0
	v_mov_b32_e32 v11, 0
	v_mov_b32_e32 v12, 0
	v_mov_b32_e32 v13, 0
	v_mov_b32_e32 v14, 0
	v_mov_b32_e32 v15, 0
	v_mov_b32_e32 v16, 0
	v_mov_b32_e32 v17, 0
	v_mov_b32_e32 v50, 0
	v_mov_b32_e32 v51, 0
	v_mov_b32_e32 v52, 0
	v_mov_b32_e32 v53, 0
	v_mov_b32_e32 v54, 0
	v_mov_b32_e32 v55, 0
	v_mov_b32_e32 v56, 0
	v_mov_b32_e32 v57, 0
	v_mov_b32_e32 v58, 0
	v_mov_b32_e32 v59, 0
	v_mov_b32_e32 v60, 0
	v_mov_b32_e32 v61, 0
	v_mov_b32_e32 v62, 0
	v_mov_b32_e32 v63, 0
	v_mov_b32_e32 v64, 0
	v_mov_b32_e32 v65, 0
	v_mov_b32_e32 v18, 0
	v_mov_b32_e32 v19, 0
	v_mov_b32_e32 v20, 0
	v_mov_b32_e32 v21, 0
	v_mov_b32_e32 v22, 0
	v_mov_b32_e32 v23, 0
	v_mov_b32_e32 v24, 0
	v_mov_b32_e32 v25, 0
	v_mov_b32_e32 v26, 0
	v_mov_b32_e32 v27, 0
	v_mov_b32_e32 v28, 0
	v_mov_b32_e32 v29, 0
	v_mov_b32_e32 v30, 0
	v_mov_b32_e32 v31, 0
	v_mov_b32_e32 v32, 0
	v_mov_b32_e32 v33, 0
	v_mov_b32_e32 v66, 0
	v_mov_b32_e32 v67, 0
	v_mov_b32_e32 v68, 0
	v_mov_b32_e32 v69, 0
	v_mov_b32_e32 v70, 0
	v_mov_b32_e32 v71, 0
	v_mov_b32_e32 v72, 0
	v_mov_b32_e32 v73, 0
	v_mov_b32_e32 v74, 0
	v_mov_b32_e32 v75, 0
	v_mov_b32_e32 v76, 0
	v_mov_b32_e32 v77, 0
	v_mov_b32_e32 v78, 0
	v_mov_b32_e32 v79, 0
	v_mov_b32_e32 v80, 0
	v_mov_b32_e32 v81, 0
	v_mov_b32_e32 v34, 0
	v_mov_b32_e32 v35, 0
	v_mov_b32_e32 v36, 0
	v_mov_b32_e32 v37, 0
	v_mov_b32_e32 v38, 0
	v_mov_b32_e32 v39, 0
	v_mov_b32_e32 v40, 0
	v_mov_b32_e32 v41, 0
	v_mov_b32_e32 v42, 0
	v_mov_b32_e32 v43, 0
	v_mov_b32_e32 v44, 0
	v_mov_b32_e32 v45, 0
	v_mov_b32_e32 v46, 0
	v_mov_b32_e32 v47, 0
	v_mov_b32_e32 v48, 0
	v_mov_b32_e32 v49, 0
	v_mov_b32_e32 v82, 0
	v_mov_b32_e32 v83, 0
	v_mov_b32_e32 v84, 0
	v_mov_b32_e32 v85, 0
	v_mov_b32_e32 v86, 0
	v_mov_b32_e32 v87, 0
	v_mov_b32_e32 v88, 0
	v_mov_b32_e32 v89, 0
	v_mov_b32_e32 v90, 0
	v_mov_b32_e32 v91, 0
	v_mov_b32_e32 v92, 0
	v_mov_b32_e32 v93, 0
	v_mov_b32_e32 v94, 0
	v_mov_b32_e32 v95, 0
	v_mov_b32_e32 v96, 0
	v_mov_b32_e32 v97, 0
	v_or_b32_e32 v99, s24, v1
	v_or_b32_e32 v100, s23, v1
	s_cbranch_scc1 .LBB1_35
	v_bfe_u32 v109, v0, 2, 2
	v_xor_b32_e32 v110, v109, v98
	v_xor_b32_e32 v111, 2, v110
	v_lshlrev_b32_e32 v110, 4, v110
	v_lshlrev_b32_e32 v111, 4, v111
	v_lshl_add_u32 v101, v99, 6, v110
	v_lshl_add_u32 v102, v99, 6, v111
	v_lshl_add_u32 v103, v100, 6, v110
	v_lshl_add_u32 v104, v100, 6, v111
	v_add_u32_e32 v101, 0x800, v101
	v_add_u32_e32 v102, 0x800, v102
	v_add_u32_e32 v103, 0x3800, v103
	v_add_u32_e32 v104, 0x3800, v104
	v_add_u32_e32 v105, 0xe000, v101
	v_add_u32_e32 v106, 0xe000, v102
	v_add_u32_e32 v107, 0xe000, v103
	v_add_u32_e32 v108, 0xe000, v104
	v_add_u32_e32 v152, 0x1c000, v101
	v_add_u32_e32 v153, 0x1c000, v102
	v_add_u32_e32 v154, 0x1c000, v103
	v_add_u32_e32 v155, 0x1c000, v104
	s_cmp_lt_u32 s2, 64
	s_cbranch_scc1 .Lqkv_cv
	s_barrier
	ds_read_b128 v[124:127], v103
	ds_read_b128 v[112:115], v101
	ds_read_b128 v[128:131], v103 offset:2048
	ds_read_b128 v[116:119], v101 offset:2048
	ds_read_b128 v[120:123], v101 offset:4096
	s_waitcnt lgkmcnt(0)
	v_mfma_f32_32x32x16_f16 v[82:97], v[112:115], v[124:127], v[82:97]
	ds_read_b128 v[144:147], v104
	ds_read_b128 v[132:135], v102
	v_mfma_f32_32x32x16_f16 v[34:49], v[112:115], v[128:131], v[34:49]
	ds_read_b128 v[148:151], v104 offset:2048
	ds_read_b128 v[136:139], v102 offset:2048
	v_mfma_f32_32x32x16_f16 v[66:81], v[116:119], v[124:127], v[66:81]
	ds_read_b128 v[140:143], v102 offset:4096
	v_mfma_f32_32x32x16_f16 v[18:33], v[116:119], v[128:131], v[18:33]
	v_mfma_f32_32x32x16_f16 v[50:65], v[120:123], v[124:127], v[50:65]
	v_mfma_f32_32x32x16_f16 v[2:17], v[120:123], v[128:131], v[2:17]
	s_waitcnt lgkmcnt(0)
	s_barrier
	v_mfma_f32_32x32x16_f16 v[82:97], v[132:135], v[144:147], v[82:97]
	ds_read_b128 v[124:127], v103 offset:28672
	ds_read_b128 v[112:115], v101 offset:28672
	v_mfma_f32_32x32x16_f16 v[34:49], v[132:135], v[148:151], v[34:49]
	ds_read_b128 v[128:131], v103 offset:30720
	ds_read_b128 v[116:119], v101 offset:30720
	v_mfma_f32_32x32x16_f16 v[66:81], v[136:139], v[144:147], v[66:81]
	ds_read_b128 v[120:123], v101 offset:32768
	v_mfma_f32_32x32x16_f16 v[18:33], v[136:139], v[148:151], v[18:33]
	v_mfma_f32_32x32x16_f16 v[50:65], v[140:143], v[144:147], v[50:65]
	v_mfma_f32_32x32x16_f16 v[2:17], v[140:143], v[148:151], v[2:17]
	s_waitcnt lgkmcnt(3)
	v_mfma_f32_32x32x16_f16 v[82:97], v[112:115], v[124:127], v[82:97]
	ds_read_b128 v[144:147], v104 offset:28672
	ds_read_b128 v[132:135], v102 offset:28672
	s_waitcnt lgkmcnt(4)
	v_mfma_f32_32x32x16_f16 v[34:49], v[112:115], v[128:131], v[34:49]
	ds_read_b128 v[148:151], v104 offset:30720
	ds_read_b128 v[136:139], v102 offset:30720
	s_waitcnt lgkmcnt(5)
	v_mfma_f32_32x32x16_f16 v[66:81], v[116:119], v[124:127], v[66:81]
	ds_read_b128 v[140:143], v102 offset:32768
	v_mfma_f32_32x32x16_f16 v[18:33], v[116:119], v[128:131], v[18:33]
	s_waitcnt lgkmcnt(5)
	v_mfma_f32_32x32x16_f16 v[50:65], v[120:123], v[124:127], v[50:65]
	v_mfma_f32_32x32x16_f16 v[2:17], v[120:123], v[128:131], v[2:17]
	s_waitcnt lgkmcnt(0)
	s_barrier
	v_mfma_f32_32x32x16_f16 v[82:97], v[132:135], v[144:147], v[82:97]
	ds_read_b128 v[124:127], v107
	ds_read_b128 v[112:115], v105
	v_mfma_f32_32x32x16_f16 v[34:49], v[132:135], v[148:151], v[34:49]
	ds_read_b128 v[128:131], v107 offset:2048
	ds_read_b128 v[116:119], v105 offset:2048
	v_mfma_f32_32x32x16_f16 v[66:81], v[136:139], v[144:147], v[66:81]
	ds_read_b128 v[120:123], v105 offset:4096
	v_mfma_f32_32x32x16_f16 v[18:33], v[136:139], v[148:151], v[18:33]
	v_mfma_f32_32x32x16_f16 v[50:65], v[140:143], v[144:147], v[50:65]
	v_mfma_f32_32x32x16_f16 v[2:17], v[140:143], v[148:151], v[2:17]
	s_waitcnt lgkmcnt(3)
	v_mfma_f32_32x32x16_f16 v[82:97], v[112:115], v[124:127], v[82:97]
	ds_read_b128 v[144:147], v108
	ds_read_b128 v[132:135], v106
	s_waitcnt lgkmcnt(4)
	v_mfma_f32_32x32x16_f16 v[34:49], v[112:115], v[128:131], v[34:49]
	ds_read_b128 v[148:151], v108 offset:2048
	ds_read_b128 v[136:139], v106 offset:2048
	s_waitcnt lgkmcnt(5)
	v_mfma_f32_32x32x16_f16 v[66:81], v[116:119], v[124:127], v[66:81]
	ds_read_b128 v[140:143], v106 offset:4096
	v_mfma_f32_32x32x16_f16 v[18:33], v[116:119], v[128:131], v[18:33]
	s_waitcnt lgkmcnt(5)
	v_mfma_f32_32x32x16_f16 v[50:65], v[120:123], v[124:127], v[50:65]
	v_mfma_f32_32x32x16_f16 v[2:17], v[120:123], v[128:131], v[2:17]
	s_waitcnt lgkmcnt(0)
	s_barrier
	v_mfma_f32_32x32x16_f16 v[82:97], v[132:135], v[144:147], v[82:97]
	ds_read_b128 v[124:127], v107 offset:28672
	ds_read_b128 v[112:115], v105 offset:28672
	v_mfma_f32_32x32x16_f16 v[34:49], v[132:135], v[148:151], v[34:49]
	ds_read_b128 v[128:131], v107 offset:30720
	ds_read_b128 v[116:119], v105 offset:30720
	v_mfma_f32_32x32x16_f16 v[66:81], v[136:139], v[144:147], v[66:81]
	ds_read_b128 v[120:123], v105 offset:32768
	v_mfma_f32_32x32x16_f16 v[18:33], v[136:139], v[148:151], v[18:33]
	v_mfma_f32_32x32x16_f16 v[50:65], v[140:143], v[144:147], v[50:65]
	v_mfma_f32_32x32x16_f16 v[2:17], v[140:143], v[148:151], v[2:17]
	s_waitcnt lgkmcnt(3)
	v_mfma_f32_32x32x16_f16 v[82:97], v[112:115], v[124:127], v[82:97]
	ds_read_b128 v[144:147], v108 offset:28672
	ds_read_b128 v[132:135], v106 offset:28672
	s_waitcnt lgkmcnt(4)
	v_mfma_f32_32x32x16_f16 v[34:49], v[112:115], v[128:131], v[34:49]
	ds_read_b128 v[148:151], v108 offset:30720
	ds_read_b128 v[136:139], v106 offset:30720
	s_waitcnt lgkmcnt(5)
	v_mfma_f32_32x32x16_f16 v[66:81], v[116:119], v[124:127], v[66:81]
	ds_read_b128 v[140:143], v106 offset:32768
	v_mfma_f32_32x32x16_f16 v[18:33], v[116:119], v[128:131], v[18:33]
	s_waitcnt lgkmcnt(5)
	v_mfma_f32_32x32x16_f16 v[50:65], v[120:123], v[124:127], v[50:65]
	v_mfma_f32_32x32x16_f16 v[2:17], v[120:123], v[128:131], v[2:17]
	s_waitcnt lgkmcnt(0)
	s_barrier
	v_mfma_f32_32x32x16_f16 v[82:97], v[132:135], v[144:147], v[82:97]
	ds_read_b128 v[124:127], v154
	ds_read_b128 v[112:115], v152
	v_mfma_f32_32x32x16_f16 v[34:49], v[132:135], v[148:151], v[34:49]
	ds_read_b128 v[128:131], v154 offset:2048
	ds_read_b128 v[116:119], v152 offset:2048
	v_mfma_f32_32x32x16_f16 v[66:81], v[136:139], v[144:147], v[66:81]
	ds_read_b128 v[120:123], v152 offset:4096
	v_mfma_f32_32x32x16_f16 v[18:33], v[136:139], v[148:151], v[18:33]
	v_mfma_f32_32x32x16_f16 v[50:65], v[140:143], v[144:147], v[50:65]
	v_mfma_f32_32x32x16_f16 v[2:17], v[140:143], v[148:151], v[2:17]
	s_waitcnt lgkmcnt(3)
	v_mfma_f32_32x32x16_f16 v[82:97], v[112:115], v[124:127], v[82:97]
	ds_read_b128 v[144:147], v155
	ds_read_b128 v[132:135], v153
	s_waitcnt lgkmcnt(4)
	v_mfma_f32_32x32x16_f16 v[34:49], v[112:115], v[128:131], v[34:49]
	ds_read_b128 v[148:151], v155 offset:2048
	ds_read_b128 v[136:139], v153 offset:2048
	s_waitcnt lgkmcnt(5)
	v_mfma_f32_32x32x16_f16 v[66:81], v[116:119], v[124:127], v[66:81]
	ds_read_b128 v[140:143], v153 offset:4096
	v_mfma_f32_32x32x16_f16 v[18:33], v[116:119], v[128:131], v[18:33]
	s_waitcnt lgkmcnt(5)
	v_mfma_f32_32x32x16_f16 v[50:65], v[120:123], v[124:127], v[50:65]
	v_mfma_f32_32x32x16_f16 v[2:17], v[120:123], v[128:131], v[2:17]
	s_waitcnt lgkmcnt(0)
	s_barrier
	v_mfma_f32_32x32x16_f16 v[82:97], v[132:135], v[144:147], v[82:97]
	ds_read_b128 v[124:127], v103
	ds_read_b128 v[112:115], v101
	v_mfma_f32_32x32x16_f16 v[34:49], v[132:135], v[148:151], v[34:49]
	ds_read_b128 v[128:131], v103 offset:2048
	ds_read_b128 v[116:119], v101 offset:2048
	v_mfma_f32_32x32x16_f16 v[66:81], v[136:139], v[144:147], v[66:81]
	ds_read_b128 v[120:123], v101 offset:4096
	v_mfma_f32_32x32x16_f16 v[18:33], v[136:139], v[148:151], v[18:33]
	v_mfma_f32_32x32x16_f16 v[50:65], v[140:143], v[144:147], v[50:65]
	v_mfma_f32_32x32x16_f16 v[2:17], v[140:143], v[148:151], v[2:17]
	s_waitcnt lgkmcnt(3)
	v_mfma_f32_32x32x16_f16 v[82:97], v[112:115], v[124:127], v[82:97]
	ds_read_b128 v[144:147], v104
	ds_read_b128 v[132:135], v102
	s_waitcnt lgkmcnt(4)
	v_mfma_f32_32x32x16_f16 v[34:49], v[112:115], v[128:131], v[34:49]
	ds_read_b128 v[148:151], v104 offset:2048
	ds_read_b128 v[136:139], v102 offset:2048
	s_waitcnt lgkmcnt(5)
	v_mfma_f32_32x32x16_f16 v[66:81], v[116:119], v[124:127], v[66:81]
	ds_read_b128 v[140:143], v102 offset:4096
	v_mfma_f32_32x32x16_f16 v[18:33], v[116:119], v[128:131], v[18:33]
	s_waitcnt lgkmcnt(5)
	v_mfma_f32_32x32x16_f16 v[50:65], v[120:123], v[124:127], v[50:65]
	v_mfma_f32_32x32x16_f16 v[2:17], v[120:123], v[128:131], v[2:17]
	s_waitcnt lgkmcnt(0)
	s_barrier
	v_mfma_f32_32x32x16_f16 v[82:97], v[132:135], v[144:147], v[82:97]
	ds_read_b128 v[124:127], v103 offset:28672
	ds_read_b128 v[112:115], v101 offset:28672
	v_mfma_f32_32x32x16_f16 v[34:49], v[132:135], v[148:151], v[34:49]
	ds_read_b128 v[128:131], v103 offset:30720
	ds_read_b128 v[116:119], v101 offset:30720
	v_mfma_f32_32x32x16_f16 v[66:81], v[136:139], v[144:147], v[66:81]
	ds_read_b128 v[120:123], v101 offset:32768
	v_mfma_f32_32x32x16_f16 v[18:33], v[136:139], v[148:151], v[18:33]
	v_mfma_f32_32x32x16_f16 v[50:65], v[140:143], v[144:147], v[50:65]
	v_mfma_f32_32x32x16_f16 v[2:17], v[140:143], v[148:151], v[2:17]
	s_waitcnt lgkmcnt(3)
	v_mfma_f32_32x32x16_f16 v[82:97], v[112:115], v[124:127], v[82:97]
	ds_read_b128 v[144:147], v104 offset:28672
	ds_read_b128 v[132:135], v102 offset:28672
	s_waitcnt lgkmcnt(4)
	v_mfma_f32_32x32x16_f16 v[34:49], v[112:115], v[128:131], v[34:49]
	ds_read_b128 v[148:151], v104 offset:30720
	ds_read_b128 v[136:139], v102 offset:30720
	s_waitcnt lgkmcnt(5)
	v_mfma_f32_32x32x16_f16 v[66:81], v[116:119], v[124:127], v[66:81]
	ds_read_b128 v[140:143], v102 offset:32768
	v_mfma_f32_32x32x16_f16 v[18:33], v[116:119], v[128:131], v[18:33]
	s_waitcnt lgkmcnt(5)
	v_mfma_f32_32x32x16_f16 v[50:65], v[120:123], v[124:127], v[50:65]
	v_mfma_f32_32x32x16_f16 v[2:17], v[120:123], v[128:131], v[2:17]
	s_waitcnt lgkmcnt(0)
	s_barrier
	v_mfma_f32_32x32x16_f16 v[82:97], v[132:135], v[144:147], v[82:97]
	ds_read_b128 v[124:127], v107
	ds_read_b128 v[112:115], v105
	v_mfma_f32_32x32x16_f16 v[34:49], v[132:135], v[148:151], v[34:49]
	ds_read_b128 v[128:131], v107 offset:2048
	ds_read_b128 v[116:119], v105 offset:2048
	v_mfma_f32_32x32x16_f16 v[66:81], v[136:139], v[144:147], v[66:81]
	ds_read_b128 v[120:123], v105 offset:4096
	v_mfma_f32_32x32x16_f16 v[18:33], v[136:139], v[148:151], v[18:33]
	v_mfma_f32_32x32x16_f16 v[50:65], v[140:143], v[144:147], v[50:65]
	v_mfma_f32_32x32x16_f16 v[2:17], v[140:143], v[148:151], v[2:17]
	s_waitcnt lgkmcnt(3)
	v_mfma_f32_32x32x16_f16 v[82:97], v[112:115], v[124:127], v[82:97]
	ds_read_b128 v[144:147], v108
	ds_read_b128 v[132:135], v106
	s_waitcnt lgkmcnt(4)
	v_mfma_f32_32x32x16_f16 v[34:49], v[112:115], v[128:131], v[34:49]
	ds_read_b128 v[148:151], v108 offset:2048
	ds_read_b128 v[136:139], v106 offset:2048
	s_waitcnt lgkmcnt(5)
	v_mfma_f32_32x32x16_f16 v[66:81], v[116:119], v[124:127], v[66:81]
	ds_read_b128 v[140:143], v106 offset:4096
	v_mfma_f32_32x32x16_f16 v[18:33], v[116:119], v[128:131], v[18:33]
	s_waitcnt lgkmcnt(5)
	v_mfma_f32_32x32x16_f16 v[50:65], v[120:123], v[124:127], v[50:65]
	v_mfma_f32_32x32x16_f16 v[2:17], v[120:123], v[128:131], v[2:17]
	s_waitcnt lgkmcnt(0)
	s_barrier
	v_mfma_f32_32x32x16_f16 v[82:97], v[132:135], v[144:147], v[82:97]
	ds_read_b128 v[124:127], v107 offset:28672
	ds_read_b128 v[112:115], v105 offset:28672
	v_mfma_f32_32x32x16_f16 v[34:49], v[132:135], v[148:151], v[34:49]
	ds_read_b128 v[128:131], v107 offset:30720
	ds_read_b128 v[116:119], v105 offset:30720
	v_mfma_f32_32x32x16_f16 v[66:81], v[136:139], v[144:147], v[66:81]
	ds_read_b128 v[120:123], v105 offset:32768
	v_mfma_f32_32x32x16_f16 v[18:33], v[136:139], v[148:151], v[18:33]
	v_mfma_f32_32x32x16_f16 v[50:65], v[140:143], v[144:147], v[50:65]
	v_mfma_f32_32x32x16_f16 v[2:17], v[140:143], v[148:151], v[2:17]
	s_waitcnt lgkmcnt(3)
	v_mfma_f32_32x32x16_f16 v[82:97], v[112:115], v[124:127], v[82:97]
	ds_read_b128 v[144:147], v108 offset:28672
	ds_read_b128 v[132:135], v106 offset:28672
	s_waitcnt lgkmcnt(4)
	v_mfma_f32_32x32x16_f16 v[34:49], v[112:115], v[128:131], v[34:49]
	ds_read_b128 v[148:151], v108 offset:30720
	ds_read_b128 v[136:139], v106 offset:30720
	s_waitcnt lgkmcnt(5)
	v_mfma_f32_32x32x16_f16 v[66:81], v[116:119], v[124:127], v[66:81]
	ds_read_b128 v[140:143], v106 offset:32768
	v_mfma_f32_32x32x16_f16 v[18:33], v[116:119], v[128:131], v[18:33]
	s_waitcnt lgkmcnt(5)
	v_mfma_f32_32x32x16_f16 v[50:65], v[120:123], v[124:127], v[50:65]
	v_mfma_f32_32x32x16_f16 v[2:17], v[120:123], v[128:131], v[2:17]
	s_waitcnt lgkmcnt(0)
	s_barrier
	v_mfma_f32_32x32x16_f16 v[82:97], v[132:135], v[144:147], v[82:97]
	ds_read_b128 v[124:127], v154
	ds_read_b128 v[112:115], v152
	v_mfma_f32_32x32x16_f16 v[34:49], v[132:135], v[148:151], v[34:49]
	ds_read_b128 v[128:131], v154 offset:2048
	ds_read_b128 v[116:119], v152 offset:2048
	v_mfma_f32_32x32x16_f16 v[66:81], v[136:139], v[144:147], v[66:81]
	ds_read_b128 v[120:123], v152 offset:4096
	v_mfma_f32_32x32x16_f16 v[18:33], v[136:139], v[148:151], v[18:33]
	v_mfma_f32_32x32x16_f16 v[50:65], v[140:143], v[144:147], v[50:65]
	v_mfma_f32_32x32x16_f16 v[2:17], v[140:143], v[148:151], v[2:17]
	s_waitcnt lgkmcnt(3)
	v_mfma_f32_32x32x16_f16 v[82:97], v[112:115], v[124:127], v[82:97]
	ds_read_b128 v[144:147], v155
	ds_read_b128 v[132:135], v153
	s_waitcnt lgkmcnt(4)
	v_mfma_f32_32x32x16_f16 v[34:49], v[112:115], v[128:131], v[34:49]
	ds_read_b128 v[148:151], v155 offset:2048
	ds_read_b128 v[136:139], v153 offset:2048
	s_waitcnt lgkmcnt(5)
	v_mfma_f32_32x32x16_f16 v[66:81], v[116:119], v[124:127], v[66:81]
	ds_read_b128 v[140:143], v153 offset:4096
	v_mfma_f32_32x32x16_f16 v[18:33], v[116:119], v[128:131], v[18:33]
	s_waitcnt lgkmcnt(5)
	v_mfma_f32_32x32x16_f16 v[50:65], v[120:123], v[124:127], v[50:65]
	v_mfma_f32_32x32x16_f16 v[2:17], v[120:123], v[128:131], v[2:17]
	s_waitcnt lgkmcnt(0)
	s_barrier
	v_mfma_f32_32x32x16_f16 v[82:97], v[132:135], v[144:147], v[82:97]
	ds_read_b128 v[124:127], v103
	ds_read_b128 v[112:115], v101
	v_mfma_f32_32x32x16_f16 v[34:49], v[132:135], v[148:151], v[34:49]
	ds_read_b128 v[128:131], v103 offset:2048
	ds_read_b128 v[116:119], v101 offset:2048
	v_mfma_f32_32x32x16_f16 v[66:81], v[136:139], v[144:147], v[66:81]
	ds_read_b128 v[120:123], v101 offset:4096
	v_mfma_f32_32x32x16_f16 v[18:33], v[136:139], v[148:151], v[18:33]
	v_mfma_f32_32x32x16_f16 v[50:65], v[140:143], v[144:147], v[50:65]
	v_mfma_f32_32x32x16_f16 v[2:17], v[140:143], v[148:151], v[2:17]
	s_waitcnt lgkmcnt(3)
	v_mfma_f32_32x32x16_f16 v[82:97], v[112:115], v[124:127], v[82:97]
	ds_read_b128 v[144:147], v104
	ds_read_b128 v[132:135], v102
	s_waitcnt lgkmcnt(4)
	v_mfma_f32_32x32x16_f16 v[34:49], v[112:115], v[128:131], v[34:49]
	ds_read_b128 v[148:151], v104 offset:2048
	ds_read_b128 v[136:139], v102 offset:2048
	s_waitcnt lgkmcnt(5)
	v_mfma_f32_32x32x16_f16 v[66:81], v[116:119], v[124:127], v[66:81]
	ds_read_b128 v[140:143], v102 offset:4096
	v_mfma_f32_32x32x16_f16 v[18:33], v[116:119], v[128:131], v[18:33]
	s_waitcnt lgkmcnt(5)
	v_mfma_f32_32x32x16_f16 v[50:65], v[120:123], v[124:127], v[50:65]
	v_mfma_f32_32x32x16_f16 v[2:17], v[120:123], v[128:131], v[2:17]
	s_waitcnt lgkmcnt(0)
	s_barrier
	v_mfma_f32_32x32x16_f16 v[82:97], v[132:135], v[144:147], v[82:97]
	ds_read_b128 v[124:127], v103 offset:28672
	ds_read_b128 v[112:115], v101 offset:28672
	v_mfma_f32_32x32x16_f16 v[34:49], v[132:135], v[148:151], v[34:49]
	ds_read_b128 v[128:131], v103 offset:30720
	ds_read_b128 v[116:119], v101 offset:30720
	v_mfma_f32_32x32x16_f16 v[66:81], v[136:139], v[144:147], v[66:81]
	ds_read_b128 v[120:123], v101 offset:32768
	v_mfma_f32_32x32x16_f16 v[18:33], v[136:139], v[148:151], v[18:33]
	v_mfma_f32_32x32x16_f16 v[50:65], v[140:143], v[144:147], v[50:65]
	v_mfma_f32_32x32x16_f16 v[2:17], v[140:143], v[148:151], v[2:17]
	s_waitcnt lgkmcnt(3)
	v_mfma_f32_32x32x16_f16 v[82:97], v[112:115], v[124:127], v[82:97]
	ds_read_b128 v[144:147], v104 offset:28672
	ds_read_b128 v[132:135], v102 offset:28672
	s_waitcnt lgkmcnt(4)
	v_mfma_f32_32x32x16_f16 v[34:49], v[112:115], v[128:131], v[34:49]
	ds_read_b128 v[148:151], v104 offset:30720
	ds_read_b128 v[136:139], v102 offset:30720
	s_waitcnt lgkmcnt(5)
	v_mfma_f32_32x32x16_f16 v[66:81], v[116:119], v[124:127], v[66:81]
	ds_read_b128 v[140:143], v102 offset:32768
	v_mfma_f32_32x32x16_f16 v[18:33], v[116:119], v[128:131], v[18:33]
	s_waitcnt lgkmcnt(5)
	v_mfma_f32_32x32x16_f16 v[50:65], v[120:123], v[124:127], v[50:65]
	v_mfma_f32_32x32x16_f16 v[2:17], v[120:123], v[128:131], v[2:17]
	s_waitcnt lgkmcnt(0)
	s_barrier
	v_mfma_f32_32x32x16_f16 v[82:97], v[132:135], v[144:147], v[82:97]
	ds_read_b128 v[124:127], v107
	ds_read_b128 v[112:115], v105
	v_mfma_f32_32x32x16_f16 v[34:49], v[132:135], v[148:151], v[34:49]
	ds_read_b128 v[128:131], v107 offset:2048
	ds_read_b128 v[116:119], v105 offset:2048
	v_mfma_f32_32x32x16_f16 v[66:81], v[136:139], v[144:147], v[66:81]
	ds_read_b128 v[120:123], v105 offset:4096
	v_mfma_f32_32x32x16_f16 v[18:33], v[136:139], v[148:151], v[18:33]
	v_mfma_f32_32x32x16_f16 v[50:65], v[140:143], v[144:147], v[50:65]
	v_mfma_f32_32x32x16_f16 v[2:17], v[140:143], v[148:151], v[2:17]
	s_waitcnt lgkmcnt(3)
	v_mfma_f32_32x32x16_f16 v[82:97], v[112:115], v[124:127], v[82:97]
	ds_read_b128 v[144:147], v108
	ds_read_b128 v[132:135], v106
	s_waitcnt lgkmcnt(4)
	v_mfma_f32_32x32x16_f16 v[34:49], v[112:115], v[128:131], v[34:49]
	ds_read_b128 v[148:151], v108 offset:2048
	ds_read_b128 v[136:139], v106 offset:2048
	s_waitcnt lgkmcnt(5)
	v_mfma_f32_32x32x16_f16 v[66:81], v[116:119], v[124:127], v[66:81]
	ds_read_b128 v[140:143], v106 offset:4096
	v_mfma_f32_32x32x16_f16 v[18:33], v[116:119], v[128:131], v[18:33]
	s_waitcnt lgkmcnt(5)
	v_mfma_f32_32x32x16_f16 v[50:65], v[120:123], v[124:127], v[50:65]
	v_mfma_f32_32x32x16_f16 v[2:17], v[120:123], v[128:131], v[2:17]
	s_waitcnt lgkmcnt(0)
	s_barrier
	v_mfma_f32_32x32x16_f16 v[82:97], v[132:135], v[144:147], v[82:97]
	ds_read_b128 v[124:127], v107 offset:28672
	ds_read_b128 v[112:115], v105 offset:28672
	v_mfma_f32_32x32x16_f16 v[34:49], v[132:135], v[148:151], v[34:49]
	ds_read_b128 v[128:131], v107 offset:30720
	ds_read_b128 v[116:119], v105 offset:30720
	v_mfma_f32_32x32x16_f16 v[66:81], v[136:139], v[144:147], v[66:81]
	ds_read_b128 v[120:123], v105 offset:32768
	v_mfma_f32_32x32x16_f16 v[18:33], v[136:139], v[148:151], v[18:33]
	v_mfma_f32_32x32x16_f16 v[50:65], v[140:143], v[144:147], v[50:65]
	v_mfma_f32_32x32x16_f16 v[2:17], v[140:143], v[148:151], v[2:17]
	s_waitcnt lgkmcnt(3)
	v_mfma_f32_32x32x16_f16 v[82:97], v[112:115], v[124:127], v[82:97]
	ds_read_b128 v[144:147], v108 offset:28672
	ds_read_b128 v[132:135], v106 offset:28672
	s_waitcnt lgkmcnt(4)
	v_mfma_f32_32x32x16_f16 v[34:49], v[112:115], v[128:131], v[34:49]
	ds_read_b128 v[148:151], v108 offset:30720
	ds_read_b128 v[136:139], v106 offset:30720
	s_waitcnt lgkmcnt(5)
	v_mfma_f32_32x32x16_f16 v[66:81], v[116:119], v[124:127], v[66:81]
	ds_read_b128 v[140:143], v106 offset:32768
	v_mfma_f32_32x32x16_f16 v[18:33], v[116:119], v[128:131], v[18:33]
	s_waitcnt lgkmcnt(5)
	v_mfma_f32_32x32x16_f16 v[50:65], v[120:123], v[124:127], v[50:65]
	v_mfma_f32_32x32x16_f16 v[2:17], v[120:123], v[128:131], v[2:17]
	s_waitcnt lgkmcnt(0)
	s_barrier
	v_mfma_f32_32x32x16_f16 v[82:97], v[132:135], v[144:147], v[82:97]
	ds_read_b128 v[124:127], v154
	ds_read_b128 v[112:115], v152
	v_mfma_f32_32x32x16_f16 v[34:49], v[132:135], v[148:151], v[34:49]
	ds_read_b128 v[128:131], v154 offset:2048
	ds_read_b128 v[116:119], v152 offset:2048
	v_mfma_f32_32x32x16_f16 v[66:81], v[136:139], v[144:147], v[66:81]
	ds_read_b128 v[120:123], v152 offset:4096
	v_mfma_f32_32x32x16_f16 v[18:33], v[136:139], v[148:151], v[18:33]
	v_mfma_f32_32x32x16_f16 v[50:65], v[140:143], v[144:147], v[50:65]
	v_mfma_f32_32x32x16_f16 v[2:17], v[140:143], v[148:151], v[2:17]
	s_waitcnt lgkmcnt(3)
	v_mfma_f32_32x32x16_f16 v[82:97], v[112:115], v[124:127], v[82:97]
	ds_read_b128 v[144:147], v155
	ds_read_b128 v[132:135], v153
	s_waitcnt lgkmcnt(4)
	v_mfma_f32_32x32x16_f16 v[34:49], v[112:115], v[128:131], v[34:49]
	ds_read_b128 v[148:151], v155 offset:2048
	ds_read_b128 v[136:139], v153 offset:2048
	s_waitcnt lgkmcnt(5)
	v_mfma_f32_32x32x16_f16 v[66:81], v[116:119], v[124:127], v[66:81]
	ds_read_b128 v[140:143], v153 offset:4096
	v_mfma_f32_32x32x16_f16 v[18:33], v[116:119], v[128:131], v[18:33]
	s_waitcnt lgkmcnt(5)
	v_mfma_f32_32x32x16_f16 v[50:65], v[120:123], v[124:127], v[50:65]
	v_mfma_f32_32x32x16_f16 v[2:17], v[120:123], v[128:131], v[2:17]
	s_waitcnt lgkmcnt(0)
	s_barrier
	v_mfma_f32_32x32x16_f16 v[82:97], v[132:135], v[144:147], v[82:97]
	ds_read_b128 v[124:127], v103
	ds_read_b128 v[112:115], v101
	v_mfma_f32_32x32x16_f16 v[34:49], v[132:135], v[148:151], v[34:49]
	ds_read_b128 v[128:131], v103 offset:2048
	ds_read_b128 v[116:119], v101 offset:2048
	v_mfma_f32_32x32x16_f16 v[66:81], v[136:139], v[144:147], v[66:81]
	ds_read_b128 v[120:123], v101 offset:4096
	v_mfma_f32_32x32x16_f16 v[18:33], v[136:139], v[148:151], v[18:33]
	v_mfma_f32_32x32x16_f16 v[50:65], v[140:143], v[144:147], v[50:65]
	v_mfma_f32_32x32x16_f16 v[2:17], v[140:143], v[148:151], v[2:17]
	s_waitcnt lgkmcnt(3)
	v_mfma_f32_32x32x16_f16 v[82:97], v[112:115], v[124:127], v[82:97]
	ds_read_b128 v[144:147], v104
	ds_read_b128 v[132:135], v102
	s_waitcnt lgkmcnt(4)
	v_mfma_f32_32x32x16_f16 v[34:49], v[112:115], v[128:131], v[34:49]
	ds_read_b128 v[148:151], v104 offset:2048
	ds_read_b128 v[136:139], v102 offset:2048
	s_waitcnt lgkmcnt(5)
	v_mfma_f32_32x32x16_f16 v[66:81], v[116:119], v[124:127], v[66:81]
	ds_read_b128 v[140:143], v102 offset:4096
	v_mfma_f32_32x32x16_f16 v[18:33], v[116:119], v[128:131], v[18:33]
	s_waitcnt lgkmcnt(5)
	v_mfma_f32_32x32x16_f16 v[50:65], v[120:123], v[124:127], v[50:65]
	v_mfma_f32_32x32x16_f16 v[2:17], v[120:123], v[128:131], v[2:17]
	s_waitcnt lgkmcnt(0)
	s_barrier
	v_mfma_f32_32x32x16_f16 v[82:97], v[132:135], v[144:147], v[82:97]
	ds_read_b128 v[124:127], v103 offset:28672
	ds_read_b128 v[112:115], v101 offset:28672
	v_mfma_f32_32x32x16_f16 v[34:49], v[132:135], v[148:151], v[34:49]
	ds_read_b128 v[128:131], v103 offset:30720
	ds_read_b128 v[116:119], v101 offset:30720
	v_mfma_f32_32x32x16_f16 v[66:81], v[136:139], v[144:147], v[66:81]
	ds_read_b128 v[120:123], v101 offset:32768
	v_mfma_f32_32x32x16_f16 v[18:33], v[136:139], v[148:151], v[18:33]
	v_mfma_f32_32x32x16_f16 v[50:65], v[140:143], v[144:147], v[50:65]
	v_mfma_f32_32x32x16_f16 v[2:17], v[140:143], v[148:151], v[2:17]
	s_waitcnt lgkmcnt(3)
	v_mfma_f32_32x32x16_f16 v[82:97], v[112:115], v[124:127], v[82:97]
	ds_read_b128 v[144:147], v104 offset:28672
	ds_read_b128 v[132:135], v102 offset:28672
	s_waitcnt lgkmcnt(4)
	v_mfma_f32_32x32x16_f16 v[34:49], v[112:115], v[128:131], v[34:49]
	ds_read_b128 v[148:151], v104 offset:30720
	ds_read_b128 v[136:139], v102 offset:30720
	s_waitcnt lgkmcnt(5)
	v_mfma_f32_32x32x16_f16 v[66:81], v[116:119], v[124:127], v[66:81]
	ds_read_b128 v[140:143], v102 offset:32768
	v_mfma_f32_32x32x16_f16 v[18:33], v[116:119], v[128:131], v[18:33]
	s_waitcnt lgkmcnt(5)
	v_mfma_f32_32x32x16_f16 v[50:65], v[120:123], v[124:127], v[50:65]
	v_mfma_f32_32x32x16_f16 v[2:17], v[120:123], v[128:131], v[2:17]
	s_waitcnt lgkmcnt(0)
	s_barrier
	v_mfma_f32_32x32x16_f16 v[82:97], v[132:135], v[144:147], v[82:97]
	ds_read_b128 v[124:127], v107
	ds_read_b128 v[112:115], v105
	v_mfma_f32_32x32x16_f16 v[34:49], v[132:135], v[148:151], v[34:49]
	ds_read_b128 v[128:131], v107 offset:2048
	ds_read_b128 v[116:119], v105 offset:2048
	v_mfma_f32_32x32x16_f16 v[66:81], v[136:139], v[144:147], v[66:81]
	ds_read_b128 v[120:123], v105 offset:4096
	v_mfma_f32_32x32x16_f16 v[18:33], v[136:139], v[148:151], v[18:33]
	v_mfma_f32_32x32x16_f16 v[50:65], v[140:143], v[144:147], v[50:65]
	v_mfma_f32_32x32x16_f16 v[2:17], v[140:143], v[148:151], v[2:17]
	s_waitcnt lgkmcnt(3)
	v_mfma_f32_32x32x16_f16 v[82:97], v[112:115], v[124:127], v[82:97]
	ds_read_b128 v[144:147], v108
	ds_read_b128 v[132:135], v106
	s_waitcnt lgkmcnt(4)
	v_mfma_f32_32x32x16_f16 v[34:49], v[112:115], v[128:131], v[34:49]
	ds_read_b128 v[148:151], v108 offset:2048
	ds_read_b128 v[136:139], v106 offset:2048
	s_waitcnt lgkmcnt(5)
	v_mfma_f32_32x32x16_f16 v[66:81], v[116:119], v[124:127], v[66:81]
	ds_read_b128 v[140:143], v106 offset:4096
	v_mfma_f32_32x32x16_f16 v[18:33], v[116:119], v[128:131], v[18:33]
	s_waitcnt lgkmcnt(5)
	v_mfma_f32_32x32x16_f16 v[50:65], v[120:123], v[124:127], v[50:65]
	v_mfma_f32_32x32x16_f16 v[2:17], v[120:123], v[128:131], v[2:17]
	s_waitcnt lgkmcnt(0)
	s_barrier
	v_mfma_f32_32x32x16_f16 v[82:97], v[132:135], v[144:147], v[82:97]
	ds_read_b128 v[124:127], v107 offset:28672
	ds_read_b128 v[112:115], v105 offset:28672
	v_mfma_f32_32x32x16_f16 v[34:49], v[132:135], v[148:151], v[34:49]
	ds_read_b128 v[128:131], v107 offset:30720
	ds_read_b128 v[116:119], v105 offset:30720
	v_mfma_f32_32x32x16_f16 v[66:81], v[136:139], v[144:147], v[66:81]
	ds_read_b128 v[120:123], v105 offset:32768
	v_mfma_f32_32x32x16_f16 v[18:33], v[136:139], v[148:151], v[18:33]
	v_mfma_f32_32x32x16_f16 v[50:65], v[140:143], v[144:147], v[50:65]
	v_mfma_f32_32x32x16_f16 v[2:17], v[140:143], v[148:151], v[2:17]
	s_waitcnt lgkmcnt(3)
	v_mfma_f32_32x32x16_f16 v[82:97], v[112:115], v[124:127], v[82:97]
	ds_read_b128 v[144:147], v108 offset:28672
	ds_read_b128 v[132:135], v106 offset:28672
	s_waitcnt lgkmcnt(4)
	v_mfma_f32_32x32x16_f16 v[34:49], v[112:115], v[128:131], v[34:49]
	ds_read_b128 v[148:151], v108 offset:30720
	ds_read_b128 v[136:139], v106 offset:30720
	s_waitcnt lgkmcnt(5)
	v_mfma_f32_32x32x16_f16 v[66:81], v[116:119], v[124:127], v[66:81]
	ds_read_b128 v[140:143], v106 offset:32768
	v_mfma_f32_32x32x16_f16 v[18:33], v[116:119], v[128:131], v[18:33]
	s_waitcnt lgkmcnt(5)
	v_mfma_f32_32x32x16_f16 v[50:65], v[120:123], v[124:127], v[50:65]
	v_mfma_f32_32x32x16_f16 v[2:17], v[120:123], v[128:131], v[2:17]
	s_waitcnt lgkmcnt(0)
	s_barrier
	v_mfma_f32_32x32x16_f16 v[82:97], v[132:135], v[144:147], v[82:97]
	ds_read_b128 v[124:127], v154
	ds_read_b128 v[112:115], v152
	v_mfma_f32_32x32x16_f16 v[34:49], v[132:135], v[148:151], v[34:49]
	ds_read_b128 v[128:131], v154 offset:2048
	ds_read_b128 v[116:119], v152 offset:2048
	v_mfma_f32_32x32x16_f16 v[66:81], v[136:139], v[144:147], v[66:81]
	ds_read_b128 v[120:123], v152 offset:4096
	v_mfma_f32_32x32x16_f16 v[18:33], v[136:139], v[148:151], v[18:33]
	v_mfma_f32_32x32x16_f16 v[50:65], v[140:143], v[144:147], v[50:65]
	v_mfma_f32_32x32x16_f16 v[2:17], v[140:143], v[148:151], v[2:17]
	s_waitcnt lgkmcnt(3)
	v_mfma_f32_32x32x16_f16 v[82:97], v[112:115], v[124:127], v[82:97]
	ds_read_b128 v[144:147], v155
	ds_read_b128 v[132:135], v153
	s_waitcnt lgkmcnt(4)
	v_mfma_f32_32x32x16_f16 v[34:49], v[112:115], v[128:131], v[34:49]
	ds_read_b128 v[148:151], v155 offset:2048
	ds_read_b128 v[136:139], v153 offset:2048
	s_waitcnt lgkmcnt(5)
	v_mfma_f32_32x32x16_f16 v[66:81], v[116:119], v[124:127], v[66:81]
	ds_read_b128 v[140:143], v153 offset:4096
	v_mfma_f32_32x32x16_f16 v[18:33], v[116:119], v[128:131], v[18:33]
	s_waitcnt lgkmcnt(5)
	v_mfma_f32_32x32x16_f16 v[50:65], v[120:123], v[124:127], v[50:65]
	v_mfma_f32_32x32x16_f16 v[2:17], v[120:123], v[128:131], v[2:17]
	s_waitcnt lgkmcnt(0)
	s_barrier
	v_mfma_f32_32x32x16_f16 v[82:97], v[132:135], v[144:147], v[82:97]
	ds_read_b128 v[124:127], v103
	ds_read_b128 v[112:115], v101
	v_mfma_f32_32x32x16_f16 v[34:49], v[132:135], v[148:151], v[34:49]
	ds_read_b128 v[128:131], v103 offset:2048
	ds_read_b128 v[116:119], v101 offset:2048
	v_mfma_f32_32x32x16_f16 v[66:81], v[136:139], v[144:147], v[66:81]
	ds_read_b128 v[120:123], v101 offset:4096
	v_mfma_f32_32x32x16_f16 v[18:33], v[136:139], v[148:151], v[18:33]
	v_mfma_f32_32x32x16_f16 v[50:65], v[140:143], v[144:147], v[50:65]
	v_mfma_f32_32x32x16_f16 v[2:17], v[140:143], v[148:151], v[2:17]
	s_waitcnt lgkmcnt(3)
	v_mfma_f32_32x32x16_f16 v[82:97], v[112:115], v[124:127], v[82:97]
	ds_read_b128 v[144:147], v104
	ds_read_b128 v[132:135], v102
	s_waitcnt lgkmcnt(4)
	v_mfma_f32_32x32x16_f16 v[34:49], v[112:115], v[128:131], v[34:49]
	ds_read_b128 v[148:151], v104 offset:2048
	ds_read_b128 v[136:139], v102 offset:2048
	s_waitcnt lgkmcnt(5)
	v_mfma_f32_32x32x16_f16 v[66:81], v[116:119], v[124:127], v[66:81]
	ds_read_b128 v[140:143], v102 offset:4096
	v_mfma_f32_32x32x16_f16 v[18:33], v[116:119], v[128:131], v[18:33]
	s_waitcnt lgkmcnt(5)
	v_mfma_f32_32x32x16_f16 v[50:65], v[120:123], v[124:127], v[50:65]
	v_mfma_f32_32x32x16_f16 v[2:17], v[120:123], v[128:131], v[2:17]
	s_waitcnt lgkmcnt(0)
	s_barrier
	v_mfma_f32_32x32x16_f16 v[82:97], v[132:135], v[144:147], v[82:97]
	ds_read_b128 v[124:127], v103 offset:28672
	ds_read_b128 v[112:115], v101 offset:28672
	v_mfma_f32_32x32x16_f16 v[34:49], v[132:135], v[148:151], v[34:49]
	ds_read_b128 v[128:131], v103 offset:30720
	ds_read_b128 v[116:119], v101 offset:30720
	v_mfma_f32_32x32x16_f16 v[66:81], v[136:139], v[144:147], v[66:81]
	ds_read_b128 v[120:123], v101 offset:32768
	v_mfma_f32_32x32x16_f16 v[18:33], v[136:139], v[148:151], v[18:33]
	v_mfma_f32_32x32x16_f16 v[50:65], v[140:143], v[144:147], v[50:65]
	v_mfma_f32_32x32x16_f16 v[2:17], v[140:143], v[148:151], v[2:17]
	s_waitcnt lgkmcnt(3)
	v_mfma_f32_32x32x16_f16 v[82:97], v[112:115], v[124:127], v[82:97]
	ds_read_b128 v[144:147], v104 offset:28672
	ds_read_b128 v[132:135], v102 offset:28672
	s_waitcnt lgkmcnt(4)
	v_mfma_f32_32x32x16_f16 v[34:49], v[112:115], v[128:131], v[34:49]
	ds_read_b128 v[148:151], v104 offset:30720
	ds_read_b128 v[136:139], v102 offset:30720
	s_waitcnt lgkmcnt(5)
	v_mfma_f32_32x32x16_f16 v[66:81], v[116:119], v[124:127], v[66:81]
	ds_read_b128 v[140:143], v102 offset:32768
	v_mfma_f32_32x32x16_f16 v[18:33], v[116:119], v[128:131], v[18:33]
	s_waitcnt lgkmcnt(5)
	v_mfma_f32_32x32x16_f16 v[50:65], v[120:123], v[124:127], v[50:65]
	v_mfma_f32_32x32x16_f16 v[2:17], v[120:123], v[128:131], v[2:17]
	s_waitcnt lgkmcnt(0)
	s_barrier
	v_mfma_f32_32x32x16_f16 v[82:97], v[132:135], v[144:147], v[82:97]
	ds_read_b128 v[124:127], v107
	ds_read_b128 v[112:115], v105
	v_mfma_f32_32x32x16_f16 v[34:49], v[132:135], v[148:151], v[34:49]
	ds_read_b128 v[128:131], v107 offset:2048
	ds_read_b128 v[116:119], v105 offset:2048
	v_mfma_f32_32x32x16_f16 v[66:81], v[136:139], v[144:147], v[66:81]
	ds_read_b128 v[120:123], v105 offset:4096
	v_mfma_f32_32x32x16_f16 v[18:33], v[136:139], v[148:151], v[18:33]
	v_mfma_f32_32x32x16_f16 v[50:65], v[140:143], v[144:147], v[50:65]
	v_mfma_f32_32x32x16_f16 v[2:17], v[140:143], v[148:151], v[2:17]
	s_waitcnt lgkmcnt(3)
	v_mfma_f32_32x32x16_f16 v[82:97], v[112:115], v[124:127], v[82:97]
	ds_read_b128 v[144:147], v108
	ds_read_b128 v[132:135], v106
	s_waitcnt lgkmcnt(4)
	v_mfma_f32_32x32x16_f16 v[34:49], v[112:115], v[128:131], v[34:49]
	ds_read_b128 v[148:151], v108 offset:2048
	ds_read_b128 v[136:139], v106 offset:2048
	s_waitcnt lgkmcnt(5)
	v_mfma_f32_32x32x16_f16 v[66:81], v[116:119], v[124:127], v[66:81]
	ds_read_b128 v[140:143], v106 offset:4096
	v_mfma_f32_32x32x16_f16 v[18:33], v[116:119], v[128:131], v[18:33]
	s_waitcnt lgkmcnt(5)
	v_mfma_f32_32x32x16_f16 v[50:65], v[120:123], v[124:127], v[50:65]
	v_mfma_f32_32x32x16_f16 v[2:17], v[120:123], v[128:131], v[2:17]
	s_waitcnt lgkmcnt(0)
	s_barrier
	v_mfma_f32_32x32x16_f16 v[82:97], v[132:135], v[144:147], v[82:97]
	ds_read_b128 v[124:127], v107 offset:28672
	ds_read_b128 v[112:115], v105 offset:28672
	v_mfma_f32_32x32x16_f16 v[34:49], v[132:135], v[148:151], v[34:49]
	ds_read_b128 v[128:131], v107 offset:30720
	ds_read_b128 v[116:119], v105 offset:30720
	v_mfma_f32_32x32x16_f16 v[66:81], v[136:139], v[144:147], v[66:81]
	ds_read_b128 v[120:123], v105 offset:32768
	v_mfma_f32_32x32x16_f16 v[18:33], v[136:139], v[148:151], v[18:33]
	v_mfma_f32_32x32x16_f16 v[50:65], v[140:143], v[144:147], v[50:65]
	v_mfma_f32_32x32x16_f16 v[2:17], v[140:143], v[148:151], v[2:17]
	s_waitcnt lgkmcnt(3)
	v_mfma_f32_32x32x16_f16 v[82:97], v[112:115], v[124:127], v[82:97]
	ds_read_b128 v[144:147], v108 offset:28672
	ds_read_b128 v[132:135], v106 offset:28672
	s_waitcnt lgkmcnt(4)
	v_mfma_f32_32x32x16_f16 v[34:49], v[112:115], v[128:131], v[34:49]
	ds_read_b128 v[148:151], v108 offset:30720
	ds_read_b128 v[136:139], v106 offset:30720
	s_waitcnt lgkmcnt(5)
	v_mfma_f32_32x32x16_f16 v[66:81], v[116:119], v[124:127], v[66:81]
	ds_read_b128 v[140:143], v106 offset:32768
	v_mfma_f32_32x32x16_f16 v[18:33], v[116:119], v[128:131], v[18:33]
	s_waitcnt lgkmcnt(5)
	v_mfma_f32_32x32x16_f16 v[50:65], v[120:123], v[124:127], v[50:65]
	v_mfma_f32_32x32x16_f16 v[2:17], v[120:123], v[128:131], v[2:17]
	s_waitcnt lgkmcnt(0)
	v_mfma_f32_32x32x16_f16 v[82:97], v[132:135], v[144:147], v[82:97]
	v_mfma_f32_32x32x16_f16 v[34:49], v[132:135], v[148:151], v[34:49]
	v_mfma_f32_32x32x16_f16 v[66:81], v[136:139], v[144:147], v[66:81]
	v_mfma_f32_32x32x16_f16 v[18:33], v[136:139], v[148:151], v[18:33]
	v_mfma_f32_32x32x16_f16 v[50:65], v[140:143], v[144:147], v[50:65]
	v_mfma_f32_32x32x16_f16 v[2:17], v[140:143], v[148:151], v[2:17]
	s_branch .LBB1_35
.Lqkv_cv:
	s_barrier
	ds_read_b128 v[124:127], v103
	ds_read_b128 v[112:115], v101
	ds_read_b128 v[128:131], v103 offset:2048
	ds_read_b128 v[116:119], v101 offset:2048
	ds_read_b128 v[120:123], v101 offset:4096
	s_waitcnt lgkmcnt(0)
	v_mfma_f32_32x32x16_f16 v[82:97], v[124:127], v[112:115], v[82:97]
	ds_read_b128 v[144:147], v104
	ds_read_b128 v[132:135], v102
	v_mfma_f32_32x32x16_f16 v[34:49], v[128:131], v[112:115], v[34:49]
	ds_read_b128 v[148:151], v104 offset:2048
	ds_read_b128 v[136:139], v102 offset:2048
	v_mfma_f32_32x32x16_f16 v[66:81], v[124:127], v[116:119], v[66:81]
	ds_read_b128 v[140:143], v102 offset:4096
	v_mfma_f32_32x32x16_f16 v[18:33], v[128:131], v[116:119], v[18:33]
	v_mfma_f32_32x32x16_f16 v[50:65], v[124:127], v[120:123], v[50:65]
	v_mfma_f32_32x32x16_f16 v[2:17], v[128:131], v[120:123], v[2:17]
	s_waitcnt lgkmcnt(0)
	s_barrier
	v_mfma_f32_32x32x16_f16 v[82:97], v[144:147], v[132:135], v[82:97]
	ds_read_b128 v[124:127], v103 offset:28672
	ds_read_b128 v[112:115], v101 offset:28672
	v_mfma_f32_32x32x16_f16 v[34:49], v[148:151], v[132:135], v[34:49]
	ds_read_b128 v[128:131], v103 offset:30720
	ds_read_b128 v[116:119], v101 offset:30720
	v_mfma_f32_32x32x16_f16 v[66:81], v[144:147], v[136:139], v[66:81]
	ds_read_b128 v[120:123], v101 offset:32768
	v_mfma_f32_32x32x16_f16 v[18:33], v[148:151], v[136:139], v[18:33]
	v_mfma_f32_32x32x16_f16 v[50:65], v[144:147], v[140:143], v[50:65]
	v_mfma_f32_32x32x16_f16 v[2:17], v[148:151], v[140:143], v[2:17]
	s_waitcnt lgkmcnt(3)
	v_mfma_f32_32x32x16_f16 v[82:97], v[124:127], v[112:115], v[82:97]
	ds_read_b128 v[144:147], v104 offset:28672
	ds_read_b128 v[132:135], v102 offset:28672
	s_waitcnt lgkmcnt(4)
	v_mfma_f32_32x32x16_f16 v[34:49], v[128:131], v[112:115], v[34:49]
	ds_read_b128 v[148:151], v104 offset:30720
	ds_read_b128 v[136:139], v102 offset:30720
	s_waitcnt lgkmcnt(5)
	v_mfma_f32_32x32x16_f16 v[66:81], v[124:127], v[116:119], v[66:81]
	ds_read_b128 v[140:143], v102 offset:32768
	v_mfma_f32_32x32x16_f16 v[18:33], v[128:131], v[116:119], v[18:33]
	s_waitcnt lgkmcnt(5)
	v_mfma_f32_32x32x16_f16 v[50:65], v[124:127], v[120:123], v[50:65]
	v_mfma_f32_32x32x16_f16 v[2:17], v[128:131], v[120:123], v[2:17]
	s_waitcnt lgkmcnt(0)
	s_barrier
	v_mfma_f32_32x32x16_f16 v[82:97], v[144:147], v[132:135], v[82:97]
	ds_read_b128 v[124:127], v107
	ds_read_b128 v[112:115], v105
	v_mfma_f32_32x32x16_f16 v[34:49], v[148:151], v[132:135], v[34:49]
	ds_read_b128 v[128:131], v107 offset:2048
	ds_read_b128 v[116:119], v105 offset:2048
	v_mfma_f32_32x32x16_f16 v[66:81], v[144:147], v[136:139], v[66:81]
	ds_read_b128 v[120:123], v105 offset:4096
	v_mfma_f32_32x32x16_f16 v[18:33], v[148:151], v[136:139], v[18:33]
	v_mfma_f32_32x32x16_f16 v[50:65], v[144:147], v[140:143], v[50:65]
	v_mfma_f32_32x32x16_f16 v[2:17], v[148:151], v[140:143], v[2:17]
	s_waitcnt lgkmcnt(3)
	v_mfma_f32_32x32x16_f16 v[82:97], v[124:127], v[112:115], v[82:97]
	ds_read_b128 v[144:147], v108
	ds_read_b128 v[132:135], v106
	s_waitcnt lgkmcnt(4)
	v_mfma_f32_32x32x16_f16 v[34:49], v[128:131], v[112:115], v[34:49]
	ds_read_b128 v[148:151], v108 offset:2048
	ds_read_b128 v[136:139], v106 offset:2048
	s_waitcnt lgkmcnt(5)
	v_mfma_f32_32x32x16_f16 v[66:81], v[124:127], v[116:119], v[66:81]
	ds_read_b128 v[140:143], v106 offset:4096
	v_mfma_f32_32x32x16_f16 v[18:33], v[128:131], v[116:119], v[18:33]
	s_waitcnt lgkmcnt(5)
	v_mfma_f32_32x32x16_f16 v[50:65], v[124:127], v[120:123], v[50:65]
	v_mfma_f32_32x32x16_f16 v[2:17], v[128:131], v[120:123], v[2:17]
	s_waitcnt lgkmcnt(0)
	s_barrier
	v_mfma_f32_32x32x16_f16 v[82:97], v[144:147], v[132:135], v[82:97]
	ds_read_b128 v[124:127], v107 offset:28672
	ds_read_b128 v[112:115], v105 offset:28672
	v_mfma_f32_32x32x16_f16 v[34:49], v[148:151], v[132:135], v[34:49]
	ds_read_b128 v[128:131], v107 offset:30720
	ds_read_b128 v[116:119], v105 offset:30720
	v_mfma_f32_32x32x16_f16 v[66:81], v[144:147], v[136:139], v[66:81]
	ds_read_b128 v[120:123], v105 offset:32768
	v_mfma_f32_32x32x16_f16 v[18:33], v[148:151], v[136:139], v[18:33]
	v_mfma_f32_32x32x16_f16 v[50:65], v[144:147], v[140:143], v[50:65]
	v_mfma_f32_32x32x16_f16 v[2:17], v[148:151], v[140:143], v[2:17]
	s_waitcnt lgkmcnt(3)
	v_mfma_f32_32x32x16_f16 v[82:97], v[124:127], v[112:115], v[82:97]
	ds_read_b128 v[144:147], v108 offset:28672
	ds_read_b128 v[132:135], v106 offset:28672
	s_waitcnt lgkmcnt(4)
	v_mfma_f32_32x32x16_f16 v[34:49], v[128:131], v[112:115], v[34:49]
	ds_read_b128 v[148:151], v108 offset:30720
	ds_read_b128 v[136:139], v106 offset:30720
	s_waitcnt lgkmcnt(5)
	v_mfma_f32_32x32x16_f16 v[66:81], v[124:127], v[116:119], v[66:81]
	ds_read_b128 v[140:143], v106 offset:32768
	v_mfma_f32_32x32x16_f16 v[18:33], v[128:131], v[116:119], v[18:33]
	s_waitcnt lgkmcnt(5)
	v_mfma_f32_32x32x16_f16 v[50:65], v[124:127], v[120:123], v[50:65]
	v_mfma_f32_32x32x16_f16 v[2:17], v[128:131], v[120:123], v[2:17]
	s_waitcnt lgkmcnt(0)
	s_barrier
	v_mfma_f32_32x32x16_f16 v[82:97], v[144:147], v[132:135], v[82:97]
	ds_read_b128 v[124:127], v154
	ds_read_b128 v[112:115], v152
	v_mfma_f32_32x32x16_f16 v[34:49], v[148:151], v[132:135], v[34:49]
	ds_read_b128 v[128:131], v154 offset:2048
	ds_read_b128 v[116:119], v152 offset:2048
	v_mfma_f32_32x32x16_f16 v[66:81], v[144:147], v[136:139], v[66:81]
	ds_read_b128 v[120:123], v152 offset:4096
	v_mfma_f32_32x32x16_f16 v[18:33], v[148:151], v[136:139], v[18:33]
	v_mfma_f32_32x32x16_f16 v[50:65], v[144:147], v[140:143], v[50:65]
	v_mfma_f32_32x32x16_f16 v[2:17], v[148:151], v[140:143], v[2:17]
	s_waitcnt lgkmcnt(3)
	v_mfma_f32_32x32x16_f16 v[82:97], v[124:127], v[112:115], v[82:97]
	ds_read_b128 v[144:147], v155
	ds_read_b128 v[132:135], v153
	s_waitcnt lgkmcnt(4)
	v_mfma_f32_32x32x16_f16 v[34:49], v[128:131], v[112:115], v[34:49]
	ds_read_b128 v[148:151], v155 offset:2048
	ds_read_b128 v[136:139], v153 offset:2048
	s_waitcnt lgkmcnt(5)
	v_mfma_f32_32x32x16_f16 v[66:81], v[124:127], v[116:119], v[66:81]
	ds_read_b128 v[140:143], v153 offset:4096
	v_mfma_f32_32x32x16_f16 v[18:33], v[128:131], v[116:119], v[18:33]
	s_waitcnt lgkmcnt(5)
	v_mfma_f32_32x32x16_f16 v[50:65], v[124:127], v[120:123], v[50:65]
	v_mfma_f32_32x32x16_f16 v[2:17], v[128:131], v[120:123], v[2:17]
	s_waitcnt lgkmcnt(0)
	s_barrier
	v_mfma_f32_32x32x16_f16 v[82:97], v[144:147], v[132:135], v[82:97]
	ds_read_b128 v[124:127], v103
	ds_read_b128 v[112:115], v101
	v_mfma_f32_32x32x16_f16 v[34:49], v[148:151], v[132:135], v[34:49]
	ds_read_b128 v[128:131], v103 offset:2048
	ds_read_b128 v[116:119], v101 offset:2048
	v_mfma_f32_32x32x16_f16 v[66:81], v[144:147], v[136:139], v[66:81]
	ds_read_b128 v[120:123], v101 offset:4096
	v_mfma_f32_32x32x16_f16 v[18:33], v[148:151], v[136:139], v[18:33]
	v_mfma_f32_32x32x16_f16 v[50:65], v[144:147], v[140:143], v[50:65]
	v_mfma_f32_32x32x16_f16 v[2:17], v[148:151], v[140:143], v[2:17]
	s_waitcnt lgkmcnt(3)
	v_mfma_f32_32x32x16_f16 v[82:97], v[124:127], v[112:115], v[82:97]
	ds_read_b128 v[144:147], v104
	ds_read_b128 v[132:135], v102
	s_waitcnt lgkmcnt(4)
	v_mfma_f32_32x32x16_f16 v[34:49], v[128:131], v[112:115], v[34:49]
	ds_read_b128 v[148:151], v104 offset:2048
	ds_read_b128 v[136:139], v102 offset:2048
	s_waitcnt lgkmcnt(5)
	v_mfma_f32_32x32x16_f16 v[66:81], v[124:127], v[116:119], v[66:81]
	ds_read_b128 v[140:143], v102 offset:4096
	v_mfma_f32_32x32x16_f16 v[18:33], v[128:131], v[116:119], v[18:33]
	s_waitcnt lgkmcnt(5)
	v_mfma_f32_32x32x16_f16 v[50:65], v[124:127], v[120:123], v[50:65]
	v_mfma_f32_32x32x16_f16 v[2:17], v[128:131], v[120:123], v[2:17]
	s_waitcnt lgkmcnt(0)
	s_barrier
	v_mfma_f32_32x32x16_f16 v[82:97], v[144:147], v[132:135], v[82:97]
	ds_read_b128 v[124:127], v103 offset:28672
	ds_read_b128 v[112:115], v101 offset:28672
	v_mfma_f32_32x32x16_f16 v[34:49], v[148:151], v[132:135], v[34:49]
	ds_read_b128 v[128:131], v103 offset:30720
	ds_read_b128 v[116:119], v101 offset:30720
	v_mfma_f32_32x32x16_f16 v[66:81], v[144:147], v[136:139], v[66:81]
	ds_read_b128 v[120:123], v101 offset:32768
	v_mfma_f32_32x32x16_f16 v[18:33], v[148:151], v[136:139], v[18:33]
	v_mfma_f32_32x32x16_f16 v[50:65], v[144:147], v[140:143], v[50:65]
	v_mfma_f32_32x32x16_f16 v[2:17], v[148:151], v[140:143], v[2:17]
	s_waitcnt lgkmcnt(3)
	v_mfma_f32_32x32x16_f16 v[82:97], v[124:127], v[112:115], v[82:97]
	ds_read_b128 v[144:147], v104 offset:28672
	ds_read_b128 v[132:135], v102 offset:28672
	s_waitcnt lgkmcnt(4)
	v_mfma_f32_32x32x16_f16 v[34:49], v[128:131], v[112:115], v[34:49]
	ds_read_b128 v[148:151], v104 offset:30720
	ds_read_b128 v[136:139], v102 offset:30720
	s_waitcnt lgkmcnt(5)
	v_mfma_f32_32x32x16_f16 v[66:81], v[124:127], v[116:119], v[66:81]
	ds_read_b128 v[140:143], v102 offset:32768
	v_mfma_f32_32x32x16_f16 v[18:33], v[128:131], v[116:119], v[18:33]
	s_waitcnt lgkmcnt(5)
	v_mfma_f32_32x32x16_f16 v[50:65], v[124:127], v[120:123], v[50:65]
	v_mfma_f32_32x32x16_f16 v[2:17], v[128:131], v[120:123], v[2:17]
	s_waitcnt lgkmcnt(0)
	s_barrier
	v_mfma_f32_32x32x16_f16 v[82:97], v[144:147], v[132:135], v[82:97]
	ds_read_b128 v[124:127], v107
	ds_read_b128 v[112:115], v105
	v_mfma_f32_32x32x16_f16 v[34:49], v[148:151], v[132:135], v[34:49]
	ds_read_b128 v[128:131], v107 offset:2048
	ds_read_b128 v[116:119], v105 offset:2048
	v_mfma_f32_32x32x16_f16 v[66:81], v[144:147], v[136:139], v[66:81]
	ds_read_b128 v[120:123], v105 offset:4096
	v_mfma_f32_32x32x16_f16 v[18:33], v[148:151], v[136:139], v[18:33]
	v_mfma_f32_32x32x16_f16 v[50:65], v[144:147], v[140:143], v[50:65]
	v_mfma_f32_32x32x16_f16 v[2:17], v[148:151], v[140:143], v[2:17]
	s_waitcnt lgkmcnt(3)
	v_mfma_f32_32x32x16_f16 v[82:97], v[124:127], v[112:115], v[82:97]
	ds_read_b128 v[144:147], v108
	ds_read_b128 v[132:135], v106
	s_waitcnt lgkmcnt(4)
	v_mfma_f32_32x32x16_f16 v[34:49], v[128:131], v[112:115], v[34:49]
	ds_read_b128 v[148:151], v108 offset:2048
	ds_read_b128 v[136:139], v106 offset:2048
	s_waitcnt lgkmcnt(5)
	v_mfma_f32_32x32x16_f16 v[66:81], v[124:127], v[116:119], v[66:81]
	ds_read_b128 v[140:143], v106 offset:4096
	v_mfma_f32_32x32x16_f16 v[18:33], v[128:131], v[116:119], v[18:33]
	s_waitcnt lgkmcnt(5)
	v_mfma_f32_32x32x16_f16 v[50:65], v[124:127], v[120:123], v[50:65]
	v_mfma_f32_32x32x16_f16 v[2:17], v[128:131], v[120:123], v[2:17]
	s_waitcnt lgkmcnt(0)
	s_barrier
	v_mfma_f32_32x32x16_f16 v[82:97], v[144:147], v[132:135], v[82:97]
	ds_read_b128 v[124:127], v107 offset:28672
	ds_read_b128 v[112:115], v105 offset:28672
	v_mfma_f32_32x32x16_f16 v[34:49], v[148:151], v[132:135], v[34:49]
	ds_read_b128 v[128:131], v107 offset:30720
	ds_read_b128 v[116:119], v105 offset:30720
	v_mfma_f32_32x32x16_f16 v[66:81], v[144:147], v[136:139], v[66:81]
	ds_read_b128 v[120:123], v105 offset:32768
	v_mfma_f32_32x32x16_f16 v[18:33], v[148:151], v[136:139], v[18:33]
	v_mfma_f32_32x32x16_f16 v[50:65], v[144:147], v[140:143], v[50:65]
	v_mfma_f32_32x32x16_f16 v[2:17], v[148:151], v[140:143], v[2:17]
	s_waitcnt lgkmcnt(3)
	v_mfma_f32_32x32x16_f16 v[82:97], v[124:127], v[112:115], v[82:97]
	ds_read_b128 v[144:147], v108 offset:28672
	ds_read_b128 v[132:135], v106 offset:28672
	s_waitcnt lgkmcnt(4)
	v_mfma_f32_32x32x16_f16 v[34:49], v[128:131], v[112:115], v[34:49]
	ds_read_b128 v[148:151], v108 offset:30720
	ds_read_b128 v[136:139], v106 offset:30720
	s_waitcnt lgkmcnt(5)
	v_mfma_f32_32x32x16_f16 v[66:81], v[124:127], v[116:119], v[66:81]
	ds_read_b128 v[140:143], v106 offset:32768
	v_mfma_f32_32x32x16_f16 v[18:33], v[128:131], v[116:119], v[18:33]
	s_waitcnt lgkmcnt(5)
	v_mfma_f32_32x32x16_f16 v[50:65], v[124:127], v[120:123], v[50:65]
	v_mfma_f32_32x32x16_f16 v[2:17], v[128:131], v[120:123], v[2:17]
	s_waitcnt lgkmcnt(0)
	s_barrier
	v_mfma_f32_32x32x16_f16 v[82:97], v[144:147], v[132:135], v[82:97]
	ds_read_b128 v[124:127], v154
	ds_read_b128 v[112:115], v152
	v_mfma_f32_32x32x16_f16 v[34:49], v[148:151], v[132:135], v[34:49]
	ds_read_b128 v[128:131], v154 offset:2048
	ds_read_b128 v[116:119], v152 offset:2048
	v_mfma_f32_32x32x16_f16 v[66:81], v[144:147], v[136:139], v[66:81]
	ds_read_b128 v[120:123], v152 offset:4096
	v_mfma_f32_32x32x16_f16 v[18:33], v[148:151], v[136:139], v[18:33]
	v_mfma_f32_32x32x16_f16 v[50:65], v[144:147], v[140:143], v[50:65]
	v_mfma_f32_32x32x16_f16 v[2:17], v[148:151], v[140:143], v[2:17]
	s_waitcnt lgkmcnt(3)
	v_mfma_f32_32x32x16_f16 v[82:97], v[124:127], v[112:115], v[82:97]
	ds_read_b128 v[144:147], v155
	ds_read_b128 v[132:135], v153
	s_waitcnt lgkmcnt(4)
	v_mfma_f32_32x32x16_f16 v[34:49], v[128:131], v[112:115], v[34:49]
	ds_read_b128 v[148:151], v155 offset:2048
	ds_read_b128 v[136:139], v153 offset:2048
	s_waitcnt lgkmcnt(5)
	v_mfma_f32_32x32x16_f16 v[66:81], v[124:127], v[116:119], v[66:81]
	ds_read_b128 v[140:143], v153 offset:4096
	v_mfma_f32_32x32x16_f16 v[18:33], v[128:131], v[116:119], v[18:33]
	s_waitcnt lgkmcnt(5)
	v_mfma_f32_32x32x16_f16 v[50:65], v[124:127], v[120:123], v[50:65]
	v_mfma_f32_32x32x16_f16 v[2:17], v[128:131], v[120:123], v[2:17]
	s_waitcnt lgkmcnt(0)
	s_barrier
	v_mfma_f32_32x32x16_f16 v[82:97], v[144:147], v[132:135], v[82:97]
	ds_read_b128 v[124:127], v103
	ds_read_b128 v[112:115], v101
	v_mfma_f32_32x32x16_f16 v[34:49], v[148:151], v[132:135], v[34:49]
	ds_read_b128 v[128:131], v103 offset:2048
	ds_read_b128 v[116:119], v101 offset:2048
	v_mfma_f32_32x32x16_f16 v[66:81], v[144:147], v[136:139], v[66:81]
	ds_read_b128 v[120:123], v101 offset:4096
	v_mfma_f32_32x32x16_f16 v[18:33], v[148:151], v[136:139], v[18:33]
	v_mfma_f32_32x32x16_f16 v[50:65], v[144:147], v[140:143], v[50:65]
	v_mfma_f32_32x32x16_f16 v[2:17], v[148:151], v[140:143], v[2:17]
	s_waitcnt lgkmcnt(3)
	v_mfma_f32_32x32x16_f16 v[82:97], v[124:127], v[112:115], v[82:97]
	ds_read_b128 v[144:147], v104
	ds_read_b128 v[132:135], v102
	s_waitcnt lgkmcnt(4)
	v_mfma_f32_32x32x16_f16 v[34:49], v[128:131], v[112:115], v[34:49]
	ds_read_b128 v[148:151], v104 offset:2048
	ds_read_b128 v[136:139], v102 offset:2048
	s_waitcnt lgkmcnt(5)
	v_mfma_f32_32x32x16_f16 v[66:81], v[124:127], v[116:119], v[66:81]
	ds_read_b128 v[140:143], v102 offset:4096
	v_mfma_f32_32x32x16_f16 v[18:33], v[128:131], v[116:119], v[18:33]
	s_waitcnt lgkmcnt(5)
	v_mfma_f32_32x32x16_f16 v[50:65], v[124:127], v[120:123], v[50:65]
	v_mfma_f32_32x32x16_f16 v[2:17], v[128:131], v[120:123], v[2:17]
	s_waitcnt lgkmcnt(0)
	s_barrier
	v_mfma_f32_32x32x16_f16 v[82:97], v[144:147], v[132:135], v[82:97]
	ds_read_b128 v[124:127], v103 offset:28672
	ds_read_b128 v[112:115], v101 offset:28672
	v_mfma_f32_32x32x16_f16 v[34:49], v[148:151], v[132:135], v[34:49]
	ds_read_b128 v[128:131], v103 offset:30720
	ds_read_b128 v[116:119], v101 offset:30720
	v_mfma_f32_32x32x16_f16 v[66:81], v[144:147], v[136:139], v[66:81]
	ds_read_b128 v[120:123], v101 offset:32768
	v_mfma_f32_32x32x16_f16 v[18:33], v[148:151], v[136:139], v[18:33]
	v_mfma_f32_32x32x16_f16 v[50:65], v[144:147], v[140:143], v[50:65]
	v_mfma_f32_32x32x16_f16 v[2:17], v[148:151], v[140:143], v[2:17]
	s_waitcnt lgkmcnt(3)
	v_mfma_f32_32x32x16_f16 v[82:97], v[124:127], v[112:115], v[82:97]
	ds_read_b128 v[144:147], v104 offset:28672
	ds_read_b128 v[132:135], v102 offset:28672
	s_waitcnt lgkmcnt(4)
	v_mfma_f32_32x32x16_f16 v[34:49], v[128:131], v[112:115], v[34:49]
	ds_read_b128 v[148:151], v104 offset:30720
	ds_read_b128 v[136:139], v102 offset:30720
	s_waitcnt lgkmcnt(5)
	v_mfma_f32_32x32x16_f16 v[66:81], v[124:127], v[116:119], v[66:81]
	ds_read_b128 v[140:143], v102 offset:32768
	v_mfma_f32_32x32x16_f16 v[18:33], v[128:131], v[116:119], v[18:33]
	s_waitcnt lgkmcnt(5)
	v_mfma_f32_32x32x16_f16 v[50:65], v[124:127], v[120:123], v[50:65]
	v_mfma_f32_32x32x16_f16 v[2:17], v[128:131], v[120:123], v[2:17]
	s_waitcnt lgkmcnt(0)
	s_barrier
	v_mfma_f32_32x32x16_f16 v[82:97], v[144:147], v[132:135], v[82:97]
	ds_read_b128 v[124:127], v107
	ds_read_b128 v[112:115], v105
	v_mfma_f32_32x32x16_f16 v[34:49], v[148:151], v[132:135], v[34:49]
	ds_read_b128 v[128:131], v107 offset:2048
	ds_read_b128 v[116:119], v105 offset:2048
	v_mfma_f32_32x32x16_f16 v[66:81], v[144:147], v[136:139], v[66:81]
	ds_read_b128 v[120:123], v105 offset:4096
	v_mfma_f32_32x32x16_f16 v[18:33], v[148:151], v[136:139], v[18:33]
	v_mfma_f32_32x32x16_f16 v[50:65], v[144:147], v[140:143], v[50:65]
	v_mfma_f32_32x32x16_f16 v[2:17], v[148:151], v[140:143], v[2:17]
	s_waitcnt lgkmcnt(3)
	v_mfma_f32_32x32x16_f16 v[82:97], v[124:127], v[112:115], v[82:97]
	ds_read_b128 v[144:147], v108
	ds_read_b128 v[132:135], v106
	s_waitcnt lgkmcnt(4)
	v_mfma_f32_32x32x16_f16 v[34:49], v[128:131], v[112:115], v[34:49]
	ds_read_b128 v[148:151], v108 offset:2048
	ds_read_b128 v[136:139], v106 offset:2048
	s_waitcnt lgkmcnt(5)
	v_mfma_f32_32x32x16_f16 v[66:81], v[124:127], v[116:119], v[66:81]
	ds_read_b128 v[140:143], v106 offset:4096
	v_mfma_f32_32x32x16_f16 v[18:33], v[128:131], v[116:119], v[18:33]
	s_waitcnt lgkmcnt(5)
	v_mfma_f32_32x32x16_f16 v[50:65], v[124:127], v[120:123], v[50:65]
	v_mfma_f32_32x32x16_f16 v[2:17], v[128:131], v[120:123], v[2:17]
	s_waitcnt lgkmcnt(0)
	s_barrier
	v_mfma_f32_32x32x16_f16 v[82:97], v[144:147], v[132:135], v[82:97]
	ds_read_b128 v[124:127], v107 offset:28672
	ds_read_b128 v[112:115], v105 offset:28672
	v_mfma_f32_32x32x16_f16 v[34:49], v[148:151], v[132:135], v[34:49]
	ds_read_b128 v[128:131], v107 offset:30720
	ds_read_b128 v[116:119], v105 offset:30720
	v_mfma_f32_32x32x16_f16 v[66:81], v[144:147], v[136:139], v[66:81]
	ds_read_b128 v[120:123], v105 offset:32768
	v_mfma_f32_32x32x16_f16 v[18:33], v[148:151], v[136:139], v[18:33]
	v_mfma_f32_32x32x16_f16 v[50:65], v[144:147], v[140:143], v[50:65]
	v_mfma_f32_32x32x16_f16 v[2:17], v[148:151], v[140:143], v[2:17]
	s_waitcnt lgkmcnt(3)
	v_mfma_f32_32x32x16_f16 v[82:97], v[124:127], v[112:115], v[82:97]
	ds_read_b128 v[144:147], v108 offset:28672
	ds_read_b128 v[132:135], v106 offset:28672
	s_waitcnt lgkmcnt(4)
	v_mfma_f32_32x32x16_f16 v[34:49], v[128:131], v[112:115], v[34:49]
	ds_read_b128 v[148:151], v108 offset:30720
	ds_read_b128 v[136:139], v106 offset:30720
	s_waitcnt lgkmcnt(5)
	v_mfma_f32_32x32x16_f16 v[66:81], v[124:127], v[116:119], v[66:81]
	ds_read_b128 v[140:143], v106 offset:32768
	v_mfma_f32_32x32x16_f16 v[18:33], v[128:131], v[116:119], v[18:33]
	s_waitcnt lgkmcnt(5)
	v_mfma_f32_32x32x16_f16 v[50:65], v[124:127], v[120:123], v[50:65]
	v_mfma_f32_32x32x16_f16 v[2:17], v[128:131], v[120:123], v[2:17]
	s_waitcnt lgkmcnt(0)
	s_barrier
	v_mfma_f32_32x32x16_f16 v[82:97], v[144:147], v[132:135], v[82:97]
	ds_read_b128 v[124:127], v154
	ds_read_b128 v[112:115], v152
	v_mfma_f32_32x32x16_f16 v[34:49], v[148:151], v[132:135], v[34:49]
	ds_read_b128 v[128:131], v154 offset:2048
	ds_read_b128 v[116:119], v152 offset:2048
	v_mfma_f32_32x32x16_f16 v[66:81], v[144:147], v[136:139], v[66:81]
	ds_read_b128 v[120:123], v152 offset:4096
	v_mfma_f32_32x32x16_f16 v[18:33], v[148:151], v[136:139], v[18:33]
	v_mfma_f32_32x32x16_f16 v[50:65], v[144:147], v[140:143], v[50:65]
	v_mfma_f32_32x32x16_f16 v[2:17], v[148:151], v[140:143], v[2:17]
	s_waitcnt lgkmcnt(3)
	v_mfma_f32_32x32x16_f16 v[82:97], v[124:127], v[112:115], v[82:97]
	ds_read_b128 v[144:147], v155
	ds_read_b128 v[132:135], v153
	s_waitcnt lgkmcnt(4)
	v_mfma_f32_32x32x16_f16 v[34:49], v[128:131], v[112:115], v[34:49]
	ds_read_b128 v[148:151], v155 offset:2048
	ds_read_b128 v[136:139], v153 offset:2048
	s_waitcnt lgkmcnt(5)
	v_mfma_f32_32x32x16_f16 v[66:81], v[124:127], v[116:119], v[66:81]
	ds_read_b128 v[140:143], v153 offset:4096
	v_mfma_f32_32x32x16_f16 v[18:33], v[128:131], v[116:119], v[18:33]
	s_waitcnt lgkmcnt(5)
	v_mfma_f32_32x32x16_f16 v[50:65], v[124:127], v[120:123], v[50:65]
	v_mfma_f32_32x32x16_f16 v[2:17], v[128:131], v[120:123], v[2:17]
	s_waitcnt lgkmcnt(0)
	s_barrier
	v_mfma_f32_32x32x16_f16 v[82:97], v[144:147], v[132:135], v[82:97]
	ds_read_b128 v[124:127], v103
	ds_read_b128 v[112:115], v101
	v_mfma_f32_32x32x16_f16 v[34:49], v[148:151], v[132:135], v[34:49]
	ds_read_b128 v[128:131], v103 offset:2048
	ds_read_b128 v[116:119], v101 offset:2048
	v_mfma_f32_32x32x16_f16 v[66:81], v[144:147], v[136:139], v[66:81]
	ds_read_b128 v[120:123], v101 offset:4096
	v_mfma_f32_32x32x16_f16 v[18:33], v[148:151], v[136:139], v[18:33]
	v_mfma_f32_32x32x16_f16 v[50:65], v[144:147], v[140:143], v[50:65]
	v_mfma_f32_32x32x16_f16 v[2:17], v[148:151], v[140:143], v[2:17]
	s_waitcnt lgkmcnt(3)
	v_mfma_f32_32x32x16_f16 v[82:97], v[124:127], v[112:115], v[82:97]
	ds_read_b128 v[144:147], v104
	ds_read_b128 v[132:135], v102
	s_waitcnt lgkmcnt(4)
	v_mfma_f32_32x32x16_f16 v[34:49], v[128:131], v[112:115], v[34:49]
	ds_read_b128 v[148:151], v104 offset:2048
	ds_read_b128 v[136:139], v102 offset:2048
	s_waitcnt lgkmcnt(5)
	v_mfma_f32_32x32x16_f16 v[66:81], v[124:127], v[116:119], v[66:81]
	ds_read_b128 v[140:143], v102 offset:4096
	v_mfma_f32_32x32x16_f16 v[18:33], v[128:131], v[116:119], v[18:33]
	s_waitcnt lgkmcnt(5)
	v_mfma_f32_32x32x16_f16 v[50:65], v[124:127], v[120:123], v[50:65]
	v_mfma_f32_32x32x16_f16 v[2:17], v[128:131], v[120:123], v[2:17]
	s_waitcnt lgkmcnt(0)
	s_barrier
	v_mfma_f32_32x32x16_f16 v[82:97], v[144:147], v[132:135], v[82:97]
	ds_read_b128 v[124:127], v103 offset:28672
	ds_read_b128 v[112:115], v101 offset:28672
	v_mfma_f32_32x32x16_f16 v[34:49], v[148:151], v[132:135], v[34:49]
	ds_read_b128 v[128:131], v103 offset:30720
	ds_read_b128 v[116:119], v101 offset:30720
	v_mfma_f32_32x32x16_f16 v[66:81], v[144:147], v[136:139], v[66:81]
	ds_read_b128 v[120:123], v101 offset:32768
	v_mfma_f32_32x32x16_f16 v[18:33], v[148:151], v[136:139], v[18:33]
	v_mfma_f32_32x32x16_f16 v[50:65], v[144:147], v[140:143], v[50:65]
	v_mfma_f32_32x32x16_f16 v[2:17], v[148:151], v[140:143], v[2:17]
	s_waitcnt lgkmcnt(3)
	v_mfma_f32_32x32x16_f16 v[82:97], v[124:127], v[112:115], v[82:97]
	ds_read_b128 v[144:147], v104 offset:28672
	ds_read_b128 v[132:135], v102 offset:28672
	s_waitcnt lgkmcnt(4)
	v_mfma_f32_32x32x16_f16 v[34:49], v[128:131], v[112:115], v[34:49]
	ds_read_b128 v[148:151], v104 offset:30720
	ds_read_b128 v[136:139], v102 offset:30720
	s_waitcnt lgkmcnt(5)
	v_mfma_f32_32x32x16_f16 v[66:81], v[124:127], v[116:119], v[66:81]
	ds_read_b128 v[140:143], v102 offset:32768
	v_mfma_f32_32x32x16_f16 v[18:33], v[128:131], v[116:119], v[18:33]
	s_waitcnt lgkmcnt(5)
	v_mfma_f32_32x32x16_f16 v[50:65], v[124:127], v[120:123], v[50:65]
	v_mfma_f32_32x32x16_f16 v[2:17], v[128:131], v[120:123], v[2:17]
	s_waitcnt lgkmcnt(0)
	s_barrier
	v_mfma_f32_32x32x16_f16 v[82:97], v[144:147], v[132:135], v[82:97]
	ds_read_b128 v[124:127], v107
	ds_read_b128 v[112:115], v105
	v_mfma_f32_32x32x16_f16 v[34:49], v[148:151], v[132:135], v[34:49]
	ds_read_b128 v[128:131], v107 offset:2048
	ds_read_b128 v[116:119], v105 offset:2048
	v_mfma_f32_32x32x16_f16 v[66:81], v[144:147], v[136:139], v[66:81]
	ds_read_b128 v[120:123], v105 offset:4096
	v_mfma_f32_32x32x16_f16 v[18:33], v[148:151], v[136:139], v[18:33]
	v_mfma_f32_32x32x16_f16 v[50:65], v[144:147], v[140:143], v[50:65]
	v_mfma_f32_32x32x16_f16 v[2:17], v[148:151], v[140:143], v[2:17]
	s_waitcnt lgkmcnt(3)
	v_mfma_f32_32x32x16_f16 v[82:97], v[124:127], v[112:115], v[82:97]
	ds_read_b128 v[144:147], v108
	ds_read_b128 v[132:135], v106
	s_waitcnt lgkmcnt(4)
	v_mfma_f32_32x32x16_f16 v[34:49], v[128:131], v[112:115], v[34:49]
	ds_read_b128 v[148:151], v108 offset:2048
	ds_read_b128 v[136:139], v106 offset:2048
	s_waitcnt lgkmcnt(5)
	v_mfma_f32_32x32x16_f16 v[66:81], v[124:127], v[116:119], v[66:81]
	ds_read_b128 v[140:143], v106 offset:4096
	v_mfma_f32_32x32x16_f16 v[18:33], v[128:131], v[116:119], v[18:33]
	s_waitcnt lgkmcnt(5)
	v_mfma_f32_32x32x16_f16 v[50:65], v[124:127], v[120:123], v[50:65]
	v_mfma_f32_32x32x16_f16 v[2:17], v[128:131], v[120:123], v[2:17]
	s_waitcnt lgkmcnt(0)
	s_barrier
	v_mfma_f32_32x32x16_f16 v[82:97], v[144:147], v[132:135], v[82:97]
	ds_read_b128 v[124:127], v107 offset:28672
	ds_read_b128 v[112:115], v105 offset:28672
	v_mfma_f32_32x32x16_f16 v[34:49], v[148:151], v[132:135], v[34:49]
	ds_read_b128 v[128:131], v107 offset:30720
	ds_read_b128 v[116:119], v105 offset:30720
	v_mfma_f32_32x32x16_f16 v[66:81], v[144:147], v[136:139], v[66:81]
	ds_read_b128 v[120:123], v105 offset:32768
	v_mfma_f32_32x32x16_f16 v[18:33], v[148:151], v[136:139], v[18:33]
	v_mfma_f32_32x32x16_f16 v[50:65], v[144:147], v[140:143], v[50:65]
	v_mfma_f32_32x32x16_f16 v[2:17], v[148:151], v[140:143], v[2:17]
	s_waitcnt lgkmcnt(3)
	v_mfma_f32_32x32x16_f16 v[82:97], v[124:127], v[112:115], v[82:97]
	ds_read_b128 v[144:147], v108 offset:28672
	ds_read_b128 v[132:135], v106 offset:28672
	s_waitcnt lgkmcnt(4)
	v_mfma_f32_32x32x16_f16 v[34:49], v[128:131], v[112:115], v[34:49]
	ds_read_b128 v[148:151], v108 offset:30720
	ds_read_b128 v[136:139], v106 offset:30720
	s_waitcnt lgkmcnt(5)
	v_mfma_f32_32x32x16_f16 v[66:81], v[124:127], v[116:119], v[66:81]
	ds_read_b128 v[140:143], v106 offset:32768
	v_mfma_f32_32x32x16_f16 v[18:33], v[128:131], v[116:119], v[18:33]
	s_waitcnt lgkmcnt(5)
	v_mfma_f32_32x32x16_f16 v[50:65], v[124:127], v[120:123], v[50:65]
	v_mfma_f32_32x32x16_f16 v[2:17], v[128:131], v[120:123], v[2:17]
	s_waitcnt lgkmcnt(0)
	s_barrier
	v_mfma_f32_32x32x16_f16 v[82:97], v[144:147], v[132:135], v[82:97]
	ds_read_b128 v[124:127], v154
	ds_read_b128 v[112:115], v152
	v_mfma_f32_32x32x16_f16 v[34:49], v[148:151], v[132:135], v[34:49]
	ds_read_b128 v[128:131], v154 offset:2048
	ds_read_b128 v[116:119], v152 offset:2048
	v_mfma_f32_32x32x16_f16 v[66:81], v[144:147], v[136:139], v[66:81]
	ds_read_b128 v[120:123], v152 offset:4096
	v_mfma_f32_32x32x16_f16 v[18:33], v[148:151], v[136:139], v[18:33]
	v_mfma_f32_32x32x16_f16 v[50:65], v[144:147], v[140:143], v[50:65]
	v_mfma_f32_32x32x16_f16 v[2:17], v[148:151], v[140:143], v[2:17]
	s_waitcnt lgkmcnt(3)
	v_mfma_f32_32x32x16_f16 v[82:97], v[124:127], v[112:115], v[82:97]
	ds_read_b128 v[144:147], v155
	ds_read_b128 v[132:135], v153
	s_waitcnt lgkmcnt(4)
	v_mfma_f32_32x32x16_f16 v[34:49], v[128:131], v[112:115], v[34:49]
	ds_read_b128 v[148:151], v155 offset:2048
	ds_read_b128 v[136:139], v153 offset:2048
	s_waitcnt lgkmcnt(5)
	v_mfma_f32_32x32x16_f16 v[66:81], v[124:127], v[116:119], v[66:81]
	ds_read_b128 v[140:143], v153 offset:4096
	v_mfma_f32_32x32x16_f16 v[18:33], v[128:131], v[116:119], v[18:33]
	s_waitcnt lgkmcnt(5)
	v_mfma_f32_32x32x16_f16 v[50:65], v[124:127], v[120:123], v[50:65]
	v_mfma_f32_32x32x16_f16 v[2:17], v[128:131], v[120:123], v[2:17]
	s_waitcnt lgkmcnt(0)
	s_barrier
	v_mfma_f32_32x32x16_f16 v[82:97], v[144:147], v[132:135], v[82:97]
	ds_read_b128 v[124:127], v103
	ds_read_b128 v[112:115], v101
	v_mfma_f32_32x32x16_f16 v[34:49], v[148:151], v[132:135], v[34:49]
	ds_read_b128 v[128:131], v103 offset:2048
	ds_read_b128 v[116:119], v101 offset:2048
	v_mfma_f32_32x32x16_f16 v[66:81], v[144:147], v[136:139], v[66:81]
	ds_read_b128 v[120:123], v101 offset:4096
	v_mfma_f32_32x32x16_f16 v[18:33], v[148:151], v[136:139], v[18:33]
	v_mfma_f32_32x32x16_f16 v[50:65], v[144:147], v[140:143], v[50:65]
	v_mfma_f32_32x32x16_f16 v[2:17], v[148:151], v[140:143], v[2:17]
	s_waitcnt lgkmcnt(3)
	v_mfma_f32_32x32x16_f16 v[82:97], v[124:127], v[112:115], v[82:97]
	ds_read_b128 v[144:147], v104
	ds_read_b128 v[132:135], v102
	s_waitcnt lgkmcnt(4)
	v_mfma_f32_32x32x16_f16 v[34:49], v[128:131], v[112:115], v[34:49]
	ds_read_b128 v[148:151], v104 offset:2048
	ds_read_b128 v[136:139], v102 offset:2048
	s_waitcnt lgkmcnt(5)
	v_mfma_f32_32x32x16_f16 v[66:81], v[124:127], v[116:119], v[66:81]
	ds_read_b128 v[140:143], v102 offset:4096
	v_mfma_f32_32x32x16_f16 v[18:33], v[128:131], v[116:119], v[18:33]
	s_waitcnt lgkmcnt(5)
	v_mfma_f32_32x32x16_f16 v[50:65], v[124:127], v[120:123], v[50:65]
	v_mfma_f32_32x32x16_f16 v[2:17], v[128:131], v[120:123], v[2:17]
	s_waitcnt lgkmcnt(0)
	s_barrier
	v_mfma_f32_32x32x16_f16 v[82:97], v[144:147], v[132:135], v[82:97]
	ds_read_b128 v[124:127], v103 offset:28672
	ds_read_b128 v[112:115], v101 offset:28672
	v_mfma_f32_32x32x16_f16 v[34:49], v[148:151], v[132:135], v[34:49]
	ds_read_b128 v[128:131], v103 offset:30720
	ds_read_b128 v[116:119], v101 offset:30720
	v_mfma_f32_32x32x16_f16 v[66:81], v[144:147], v[136:139], v[66:81]
	ds_read_b128 v[120:123], v101 offset:32768
	v_mfma_f32_32x32x16_f16 v[18:33], v[148:151], v[136:139], v[18:33]
	v_mfma_f32_32x32x16_f16 v[50:65], v[144:147], v[140:143], v[50:65]
	v_mfma_f32_32x32x16_f16 v[2:17], v[148:151], v[140:143], v[2:17]
	s_waitcnt lgkmcnt(3)
	v_mfma_f32_32x32x16_f16 v[82:97], v[124:127], v[112:115], v[82:97]
	ds_read_b128 v[144:147], v104 offset:28672
	ds_read_b128 v[132:135], v102 offset:28672
	s_waitcnt lgkmcnt(4)
	v_mfma_f32_32x32x16_f16 v[34:49], v[128:131], v[112:115], v[34:49]
	ds_read_b128 v[148:151], v104 offset:30720
	ds_read_b128 v[136:139], v102 offset:30720
	s_waitcnt lgkmcnt(5)
	v_mfma_f32_32x32x16_f16 v[66:81], v[124:127], v[116:119], v[66:81]
	ds_read_b128 v[140:143], v102 offset:32768
	v_mfma_f32_32x32x16_f16 v[18:33], v[128:131], v[116:119], v[18:33]
	s_waitcnt lgkmcnt(5)
	v_mfma_f32_32x32x16_f16 v[50:65], v[124:127], v[120:123], v[50:65]
	v_mfma_f32_32x32x16_f16 v[2:17], v[128:131], v[120:123], v[2:17]
	s_waitcnt lgkmcnt(0)
	s_barrier
	v_mfma_f32_32x32x16_f16 v[82:97], v[144:147], v[132:135], v[82:97]
	ds_read_b128 v[124:127], v107
	ds_read_b128 v[112:115], v105
	v_mfma_f32_32x32x16_f16 v[34:49], v[148:151], v[132:135], v[34:49]
	ds_read_b128 v[128:131], v107 offset:2048
	ds_read_b128 v[116:119], v105 offset:2048
	v_mfma_f32_32x32x16_f16 v[66:81], v[144:147], v[136:139], v[66:81]
	ds_read_b128 v[120:123], v105 offset:4096
	v_mfma_f32_32x32x16_f16 v[18:33], v[148:151], v[136:139], v[18:33]
	v_mfma_f32_32x32x16_f16 v[50:65], v[144:147], v[140:143], v[50:65]
	v_mfma_f32_32x32x16_f16 v[2:17], v[148:151], v[140:143], v[2:17]
	s_waitcnt lgkmcnt(3)
	v_mfma_f32_32x32x16_f16 v[82:97], v[124:127], v[112:115], v[82:97]
	ds_read_b128 v[144:147], v108
	ds_read_b128 v[132:135], v106
	s_waitcnt lgkmcnt(4)
	v_mfma_f32_32x32x16_f16 v[34:49], v[128:131], v[112:115], v[34:49]
	ds_read_b128 v[148:151], v108 offset:2048
	ds_read_b128 v[136:139], v106 offset:2048
	s_waitcnt lgkmcnt(5)
	v_mfma_f32_32x32x16_f16 v[66:81], v[124:127], v[116:119], v[66:81]
	ds_read_b128 v[140:143], v106 offset:4096
	v_mfma_f32_32x32x16_f16 v[18:33], v[128:131], v[116:119], v[18:33]
	s_waitcnt lgkmcnt(5)
	v_mfma_f32_32x32x16_f16 v[50:65], v[124:127], v[120:123], v[50:65]
	v_mfma_f32_32x32x16_f16 v[2:17], v[128:131], v[120:123], v[2:17]
	s_waitcnt lgkmcnt(0)
	s_barrier
	v_mfma_f32_32x32x16_f16 v[82:97], v[144:147], v[132:135], v[82:97]
	ds_read_b128 v[124:127], v107 offset:28672
	ds_read_b128 v[112:115], v105 offset:28672
	v_mfma_f32_32x32x16_f16 v[34:49], v[148:151], v[132:135], v[34:49]
	ds_read_b128 v[128:131], v107 offset:30720
	ds_read_b128 v[116:119], v105 offset:30720
	v_mfma_f32_32x32x16_f16 v[66:81], v[144:147], v[136:139], v[66:81]
	ds_read_b128 v[120:123], v105 offset:32768
	v_mfma_f32_32x32x16_f16 v[18:33], v[148:151], v[136:139], v[18:33]
	v_mfma_f32_32x32x16_f16 v[50:65], v[144:147], v[140:143], v[50:65]
	v_mfma_f32_32x32x16_f16 v[2:17], v[148:151], v[140:143], v[2:17]
	s_waitcnt lgkmcnt(3)
	v_mfma_f32_32x32x16_f16 v[82:97], v[124:127], v[112:115], v[82:97]
	ds_read_b128 v[144:147], v108 offset:28672
	ds_read_b128 v[132:135], v106 offset:28672
	s_waitcnt lgkmcnt(4)
	v_mfma_f32_32x32x16_f16 v[34:49], v[128:131], v[112:115], v[34:49]
	ds_read_b128 v[148:151], v108 offset:30720
	ds_read_b128 v[136:139], v106 offset:30720
	s_waitcnt lgkmcnt(5)
	v_mfma_f32_32x32x16_f16 v[66:81], v[124:127], v[116:119], v[66:81]
	ds_read_b128 v[140:143], v106 offset:32768
	v_mfma_f32_32x32x16_f16 v[18:33], v[128:131], v[116:119], v[18:33]
	s_waitcnt lgkmcnt(5)
	v_mfma_f32_32x32x16_f16 v[50:65], v[124:127], v[120:123], v[50:65]
	v_mfma_f32_32x32x16_f16 v[2:17], v[128:131], v[120:123], v[2:17]
	s_waitcnt lgkmcnt(0)
	v_mfma_f32_32x32x16_f16 v[82:97], v[144:147], v[132:135], v[82:97]
	v_mfma_f32_32x32x16_f16 v[34:49], v[148:151], v[132:135], v[34:49]
	v_mfma_f32_32x32x16_f16 v[66:81], v[144:147], v[136:139], v[66:81]
	v_mfma_f32_32x32x16_f16 v[18:33], v[148:151], v[136:139], v[18:33]
	v_mfma_f32_32x32x16_f16 v[50:65], v[144:147], v[140:143], v[50:65]
	v_mfma_f32_32x32x16_f16 v[2:17], v[148:151], v[140:143], v[2:17]
